# speedup vs baseline: 1.0030x; 1.0030x over previous
.LBB1_19:
	s_or_b64 exec, exec, s[30:31]
	s_mov_b64 s[30:31], 0x80
	v_readfirstlane_b32 s21, v147
	v_add_u32_e32 v160, 0x2000, v147
	v_lshl_add_u64 v[4:5], v[4:5], 0, s[30:31]
	s_mov_b32 m0, s21
	v_readfirstlane_b32 s21, v160
	v_add_u32_e32 v162, 0x8000, v144
	s_waitcnt vmcnt(4)
	s_barrier
	global_load_lds_dwordx4 v[4:5], off
	v_lshl_add_u64 v[4:5], v[6:7], 0, s[30:31]
	s_mov_b32 m0, s21
	v_readfirstlane_b32 s21, v162
	v_add_u32_e32 v163, 0xa000, v144
	global_load_lds_dwordx4 v[4:5], off
	v_lshl_add_u64 v[4:5], v[10:11], 0, s[30:31]
	s_mov_b32 m0, s21
	v_readfirstlane_b32 s21, v163
	global_load_lds_dwordx4 v[4:5], off
	v_lshl_add_u64 v[4:5], v[8:9], 0, s[30:31]
	s_mov_b32 m0, s21
	v_readfirstlane_b32 s21, v148
	v_add_u32_e32 v164, 0x2000, v148
	global_load_lds_dwordx4 v[4:5], off
	v_lshl_add_u64 v[4:5], v[12:13], 0, s[30:31]
	s_mov_b32 m0, s21
	v_readfirstlane_b32 s21, v164
	global_load_lds_dwordx4 v[4:5], off
	v_lshl_add_u64 v[4:5], v[14:15], 0, s[30:31]
	s_mov_b32 m0, s21
	s_add_u32 s26, s14, s26
	global_load_lds_dwordx4 v[4:5], off
	v_lshlrev_b32_e32 v9, 2, v204
	s_addc_u32 s27, s15, s27
	v_bfe_u32 v214, v0, 6, 2
	s_waitcnt vmcnt(6)
	v_lshlrev_b32_e32 v205, 6, v3
	v_lshlrev_b32_e32 v3, 13, v3
	v_lshl_or_b32 v8, v204, 6, v84
	v_and_b32_e32 v9, 32, v9
	v_lshl_add_u64 v[136:137], s[26:27], 0, v[72:73]
	v_lshl_add_u64 v[138:139], s[26:27], 0, v[70:71]
	s_add_u32 s26, s12, s28
	v_lshlrev_b32_e32 v4, 12, v214
	v_add_u32_e32 v5, s46, v85
	v_add_u32_e32 v6, s48, v85
	v_add_u32_e32 v7, s49, v85
	v_xad_u32 v8, v8, v9, 0
	v_or_b32_e32 v9, 0x800, v3
	v_or_b32_e32 v10, 0x1000, v3
	v_or_b32_e32 v11, 0x1800, v3
	s_addc_u32 s27, s13, s29
	v_lshl_add_u64 v[140:141], s[26:27], 0, v[72:73]
	v_lshl_add_u64 v[142:143], s[26:27], 0, v[70:71]
	s_mov_b32 s21, -2
	v_add_u32_e32 v165, v5, v4
	v_add_u32_e32 v152, v83, v3
	v_add_u32_e32 v151, v8, v9
	v_add_u32_e32 v150, v8, v10
	v_add_u32_e32 v149, v8, v11
	s_mov_b64 s[26:27], 0x80080
	v_add_u32_e32 v166, 0xc000, v144
	v_add_u32_e32 v167, 0xe000, v144
	v_add_u32_e32 v161, v82, v4
	s_mov_b64 s[28:29], 0x100
	s_mov_b64 s[30:31], 0x80100
	v_add_u32_e32 v155, v6, v4
	s_mov_b64 s[34:35], 0x180
	s_mov_b64 s[36:37], 0x80180
	v_add_u32_e32 v153, v7, v4
	v_mov_b32_e32 v3, v2
	v_mov_b32_e32 v4, v2
	v_mov_b32_e32 v5, v2
	v_mov_b32_e32 v6, v2
	v_mov_b32_e32 v7, v2
	v_mov_b32_e32 v8, v2
	v_mov_b32_e32 v9, v2
	v_mov_b32_e32 v10, v2
	v_mov_b32_e32 v11, v2
	v_mov_b32_e32 v12, v2
	v_mov_b32_e32 v13, v2
	v_mov_b32_e32 v14, v2
	v_mov_b32_e32 v15, v2
	v_mov_b32_e32 v16, v2
	v_mov_b32_e32 v17, v2
	v_mov_b32_e32 v18, v2
	v_mov_b32_e32 v19, v2
	v_mov_b32_e32 v20, v2
	v_mov_b32_e32 v21, v2
	v_mov_b32_e32 v22, v2
	v_mov_b32_e32 v23, v2
	v_mov_b32_e32 v24, v2
	v_mov_b32_e32 v25, v2
	v_mov_b32_e32 v26, v2
	v_mov_b32_e32 v27, v2
	v_mov_b32_e32 v28, v2
	v_mov_b32_e32 v29, v2
	v_mov_b32_e32 v30, v2
	v_mov_b32_e32 v31, v2
	v_mov_b32_e32 v32, v2
	v_mov_b32_e32 v33, v2
	v_mov_b32_e32 v34, v2
	v_mov_b32_e32 v35, v2
	v_mov_b32_e32 v36, v2
	v_mov_b32_e32 v37, v2
	v_mov_b32_e32 v38, v2
	v_mov_b32_e32 v39, v2
	v_mov_b32_e32 v40, v2
	v_mov_b32_e32 v41, v2
	v_mov_b32_e32 v42, v2
	v_mov_b32_e32 v43, v2
	v_mov_b32_e32 v44, v2
	v_mov_b32_e32 v45, v2
	v_mov_b32_e32 v46, v2
	v_mov_b32_e32 v47, v2
	v_mov_b32_e32 v48, v2
	v_mov_b32_e32 v49, v2
	v_mov_b32_e32 v50, v2
	v_mov_b32_e32 v51, v2
	v_mov_b32_e32 v52, v2
	v_mov_b32_e32 v53, v2
	v_mov_b32_e32 v54, v2
	v_mov_b32_e32 v55, v2
	v_mov_b32_e32 v56, v2
	v_mov_b32_e32 v57, v2
	v_mov_b32_e32 v58, v2
	v_mov_b32_e32 v59, v2
	v_mov_b32_e32 v60, v2
	v_mov_b32_e32 v61, v2
	v_mov_b32_e32 v62, v2
	v_mov_b32_e32 v63, v2
	v_mov_b32_e32 v64, v2
	v_mov_b32_e32 v65, v2
	v_mov_b32_e32 v66, v2
	v_mov_b32_e32 v67, v2
	v_mov_b32_e32 v68, v2
	v_mov_b32_e32 v69, v2
	v_mov_b32_e32 v70, v2
	v_mov_b32_e32 v71, v2
	v_mov_b32_e32 v72, v2
	v_mov_b32_e32 v73, v2
	v_mov_b32_e32 v82, v2
	v_mov_b32_e32 v83, v2
	v_mov_b32_e32 v84, v2
	v_mov_b32_e32 v85, v2
	v_mov_b32_e32 v86, v2
	v_mov_b32_e32 v87, v2
	v_mov_b32_e32 v88, v2
	v_mov_b32_e32 v89, v2
	v_mov_b32_e32 v90, v2
	v_mov_b32_e32 v91, v2
	v_mov_b32_e32 v92, v2
	v_mov_b32_e32 v93, v2
	v_mov_b32_e32 v94, v2
	v_mov_b32_e32 v95, v2
	v_mov_b32_e32 v96, v2
	v_mov_b32_e32 v97, v2
	v_mov_b32_e32 v98, v2
	v_mov_b32_e32 v99, v2
	v_mov_b32_e32 v100, v2
	v_mov_b32_e32 v101, v2
	v_mov_b32_e32 v102, v2
	v_mov_b32_e32 v103, v2
	v_mov_b32_e32 v104, v2
	v_mov_b32_e32 v105, v2
	v_mov_b32_e32 v106, v2
	v_mov_b32_e32 v107, v2
	v_mov_b32_e32 v108, v2
	v_mov_b32_e32 v109, v2
	v_mov_b32_e32 v110, v2
	v_mov_b32_e32 v111, v2
	v_mov_b32_e32 v112, v2
	v_mov_b32_e32 v113, v2
	v_mov_b32_e32 v114, v2
	v_mov_b32_e32 v115, v2
	v_mov_b32_e32 v116, v2
	v_mov_b32_e32 v117, v2
	v_mov_b32_e32 v118, v2
	v_mov_b32_e32 v119, v2
	v_mov_b32_e32 v120, v2
	v_mov_b32_e32 v121, v2
	v_mov_b32_e32 v122, v2
	v_mov_b32_e32 v123, v2
	v_mov_b32_e32 v124, v2
	v_mov_b32_e32 v125, v2
	v_mov_b32_e32 v126, v2
	v_mov_b32_e32 v127, v2
	v_mov_b32_e32 v128, v2
	v_mov_b32_e32 v129, v2
	v_mov_b32_e32 v74, v2
	v_mov_b32_e32 v75, v2
	v_mov_b32_e32 v76, v2
	v_mov_b32_e32 v77, v2
	v_mov_b32_e32 v78, v2
	v_mov_b32_e32 v79, v2
	v_mov_b32_e32 v80, v2
	v_mov_b32_e32 v81, v2
	s_barrier
	s_nop 1
	v_readfirstlane_b32 s74, v166
	v_readfirstlane_b32 s75, v167
	v_readfirstlane_b32 s76, v146
	v_readfirstlane_b32 s77, v154
	v_readfirstlane_b32 s78, v144
	v_readfirstlane_b32 s79, v156
	v_readfirstlane_b32 s80, v145
	v_readfirstlane_b32 s81, v157
	v_readfirstlane_b32 s82, v158
	v_readfirstlane_b32 s83, v159
	v_readfirstlane_b32 s84, v147
	v_readfirstlane_b32 s85, v160
	v_readfirstlane_b32 s86, v162
	v_readfirstlane_b32 s87, v163
	v_readfirstlane_b32 s88, v148
	v_readfirstlane_b32 s89, v164
.LBB1_20:
	ds_read_b128 v[168:171], v165
	ds_read_b128 v[172:175], v165 offset:1024
	ds_read_b128 v[176:179], v165 offset:2048
	ds_read_b128 v[180:183], v165 offset:3072
	v_lshl_add_u64 v[200:201], v[140:141], 0, v[130:131]
	v_lshl_add_u64 v[184:185], v[200:201], 0, s[26:27]
	s_mov_b32 m0, s74
	v_lshl_add_u64 v[206:207], v[142:143], 0, v[130:131]
	global_load_lds_dwordx4 v[184:185], off
	v_lshl_add_u64 v[184:185], v[206:207], 0, s[26:27]
	s_mov_b32 m0, s75
	s_nop 0
	global_load_lds_dwordx4 v[184:185], off
	ds_read_b128 v[184:187], v152
	ds_read_b128 v[188:191], v152 offset:1024
	ds_read_b128 v[192:195], v151
	ds_read_b128 v[196:199], v151 offset:1024
	ds_read_b128 v[216:219], v150
	ds_read_b128 v[220:223], v150 offset:1024
	ds_read_b128 v[224:227], v149
	ds_read_b128 v[228:231], v149 offset:1024
	s_waitcnt lgkmcnt(8)
	s_barrier
	s_waitcnt lgkmcnt(0)
	s_setprio 1
	s_waitcnt lgkmcnt(0)
	v_mfma_f32_16x16x32_f16 v[126:129], v[168:171], v[184:187], v[126:129]
	v_mfma_f32_16x16x32_f16 v[122:125], v[176:179], v[184:187], v[122:125]
	v_mfma_f32_16x16x32_f16 v[118:121], v[168:171], v[192:195], v[118:121]
	v_mfma_f32_16x16x32_f16 v[114:117], v[176:179], v[192:195], v[114:117]
	v_mfma_f32_16x16x32_f16 v[110:113], v[168:171], v[216:219], v[110:113]
	v_mfma_f32_16x16x32_f16 v[106:109], v[176:179], v[216:219], v[106:109]
	v_mfma_f32_16x16x32_f16 v[102:105], v[168:171], v[224:227], v[102:105]
	v_mfma_f32_16x16x32_f16 v[98:101], v[176:179], v[224:227], v[98:101]
	v_mfma_f32_16x16x32_f16 v[126:129], v[172:175], v[188:191], v[126:129]
	v_mfma_f32_16x16x32_f16 v[122:125], v[180:183], v[188:191], v[122:125]
	v_mfma_f32_16x16x32_f16 v[118:121], v[172:175], v[196:199], v[118:121]
	v_mfma_f32_16x16x32_f16 v[114:117], v[180:183], v[196:199], v[114:117]
	v_mfma_f32_16x16x32_f16 v[110:113], v[172:175], v[220:223], v[110:113]
	v_mfma_f32_16x16x32_f16 v[106:109], v[180:183], v[220:223], v[106:109]
	v_mfma_f32_16x16x32_f16 v[102:105], v[172:175], v[228:231], v[102:105]
	v_mfma_f32_16x16x32_f16 v[98:101], v[180:183], v[228:231], v[98:101]
	s_setprio 0
	s_barrier
	v_lshl_add_u64 v[248:249], v[136:137], 0, v[130:131]
	v_lshl_add_u64 v[250:251], v[248:249], 0, s[28:29]
	s_mov_b32 m0, s76
	ds_read_b128 v[232:235], v161
	ds_read_b128 v[236:239], v161 offset:1024
	ds_read_b128 v[240:243], v161 offset:2048
	ds_read_b128 v[244:247], v161 offset:3072
	global_load_lds_dwordx4 v[250:251], off
	v_lshl_add_u64 v[250:251], v[138:139], 0, v[130:131]
	v_lshl_add_u64 v[252:253], v[250:251], 0, s[28:29]
	s_mov_b32 m0, s77
	s_nop 0
	global_load_lds_dwordx4 v[252:253], off
	s_barrier
	s_waitcnt lgkmcnt(0)
	s_setprio 1
	s_waitcnt lgkmcnt(0)
	v_mfma_f32_16x16x32_f16 v[94:97], v[232:235], v[184:187], v[94:97]
	v_mfma_f32_16x16x32_f16 v[90:93], v[240:243], v[184:187], v[90:93]
	v_mfma_f32_16x16x32_f16 v[86:89], v[232:235], v[192:195], v[86:89]
	v_mfma_f32_16x16x32_f16 v[82:85], v[240:243], v[192:195], v[82:85]
	v_mfma_f32_16x16x32_f16 v[70:73], v[232:235], v[216:219], v[70:73]
	v_mfma_f32_16x16x32_f16 v[66:69], v[240:243], v[216:219], v[66:69]
	v_mfma_f32_16x16x32_f16 v[62:65], v[232:235], v[224:227], v[62:65]
	v_mfma_f32_16x16x32_f16 v[58:61], v[240:243], v[224:227], v[58:61]
	v_mfma_f32_16x16x32_f16 v[94:97], v[236:239], v[188:191], v[94:97]
	v_mfma_f32_16x16x32_f16 v[90:93], v[244:247], v[188:191], v[90:93]
	v_mfma_f32_16x16x32_f16 v[86:89], v[236:239], v[196:199], v[86:89]
	v_mfma_f32_16x16x32_f16 v[82:85], v[244:247], v[196:199], v[82:85]
	v_mfma_f32_16x16x32_f16 v[70:73], v[236:239], v[220:223], v[70:73]
	v_mfma_f32_16x16x32_f16 v[66:69], v[244:247], v[220:223], v[66:69]
	v_mfma_f32_16x16x32_f16 v[62:65], v[236:239], v[228:231], v[62:65]
	v_mfma_f32_16x16x32_f16 v[58:61], v[244:247], v[228:231], v[58:61]
	s_setprio 0
	v_lshl_add_u64 v[252:253], v[200:201], 0, s[28:29]
	s_mov_b32 m0, s78
	s_barrier
	ds_read_b128 v[184:187], v152 offset:16384
	ds_read_b128 v[188:191], v152 offset:17408
	ds_read_b128 v[192:195], v151 offset:16384
	ds_read_b128 v[196:199], v151 offset:17408
	ds_read_b128 v[216:219], v150 offset:16384
	ds_read_b128 v[220:223], v150 offset:17408
	ds_read_b128 v[224:227], v149 offset:16384
	ds_read_b128 v[228:231], v149 offset:17408
	global_load_lds_dwordx4 v[252:253], off
	v_lshl_add_u64 v[252:253], v[206:207], 0, s[28:29]
	s_mov_b32 m0, s79
	s_nop 0
	global_load_lds_dwordx4 v[252:253], off
	s_barrier
	s_waitcnt lgkmcnt(0)
	s_setprio 1
	s_waitcnt lgkmcnt(0)
	v_mfma_f32_16x16x32_f16 v[54:57], v[168:171], v[184:187], v[54:57]
	v_mfma_f32_16x16x32_f16 v[50:53], v[176:179], v[184:187], v[50:53]
	v_mfma_f32_16x16x32_f16 v[46:49], v[168:171], v[192:195], v[46:49]
	v_mfma_f32_16x16x32_f16 v[42:45], v[176:179], v[192:195], v[42:45]
	v_mfma_f32_16x16x32_f16 v[38:41], v[168:171], v[216:219], v[38:41]
	v_mfma_f32_16x16x32_f16 v[34:37], v[176:179], v[216:219], v[34:37]
	v_mfma_f32_16x16x32_f16 v[30:33], v[168:171], v[224:227], v[30:33]
	v_mfma_f32_16x16x32_f16 v[26:29], v[176:179], v[224:227], v[26:29]
	v_mfma_f32_16x16x32_f16 v[54:57], v[172:175], v[188:191], v[54:57]
	v_mfma_f32_16x16x32_f16 v[50:53], v[180:183], v[188:191], v[50:53]
	v_mfma_f32_16x16x32_f16 v[46:49], v[172:175], v[196:199], v[46:49]
	v_mfma_f32_16x16x32_f16 v[42:45], v[180:183], v[196:199], v[42:45]
	v_mfma_f32_16x16x32_f16 v[38:41], v[172:175], v[220:223], v[38:41]
	v_mfma_f32_16x16x32_f16 v[34:37], v[180:183], v[220:223], v[34:37]
	v_mfma_f32_16x16x32_f16 v[30:33], v[172:175], v[228:231], v[30:33]
	v_mfma_f32_16x16x32_f16 v[26:29], v[180:183], v[228:231], v[26:29]
	s_setprio 0
	s_barrier
	v_lshl_add_u64 v[168:169], v[248:249], 0, s[30:31]
	s_mov_b32 m0, s80
	s_nop 0
	global_load_lds_dwordx4 v[168:169], off
	v_lshl_add_u64 v[168:169], v[250:251], 0, s[30:31]
	s_mov_b32 m0, s81
	s_nop 0
	global_load_lds_dwordx4 v[168:169], off
	s_waitcnt vmcnt(6)
	s_barrier
	s_setprio 1
	v_mfma_f32_16x16x32_f16 v[22:25], v[232:235], v[184:187], v[22:25]
	v_mfma_f32_16x16x32_f16 v[18:21], v[240:243], v[184:187], v[18:21]
	v_mfma_f32_16x16x32_f16 v[14:17], v[232:235], v[192:195], v[14:17]
	v_mfma_f32_16x16x32_f16 v[10:13], v[240:243], v[192:195], v[10:13]
	v_mfma_f32_16x16x32_f16 v[6:9], v[232:235], v[216:219], v[6:9]
	v_mfma_f32_16x16x32_f16 v[2:5], v[240:243], v[216:219], v[2:5]
	v_mfma_f32_16x16x32_f16 v[74:77], v[232:235], v[224:227], v[74:77]
	v_mfma_f32_16x16x32_f16 v[78:81], v[240:243], v[224:227], v[78:81]
	v_mfma_f32_16x16x32_f16 v[22:25], v[236:239], v[188:191], v[22:25]
	v_mfma_f32_16x16x32_f16 v[18:21], v[244:247], v[188:191], v[18:21]
	v_mfma_f32_16x16x32_f16 v[14:17], v[236:239], v[196:199], v[14:17]
	v_mfma_f32_16x16x32_f16 v[10:13], v[244:247], v[196:199], v[10:13]
	v_mfma_f32_16x16x32_f16 v[6:9], v[236:239], v[220:223], v[6:9]
	v_mfma_f32_16x16x32_f16 v[2:5], v[244:247], v[220:223], v[2:5]
	v_mfma_f32_16x16x32_f16 v[74:77], v[236:239], v[228:231], v[74:77]
	v_mfma_f32_16x16x32_f16 v[78:81], v[244:247], v[228:231], v[78:81]
	s_setprio 0
	s_barrier
	ds_read_b128 v[168:171], v155
	ds_read_b128 v[172:175], v155 offset:1024
	ds_read_b128 v[176:179], v155 offset:2048
	ds_read_b128 v[180:183], v155 offset:3072
	v_lshl_add_u64 v[232:233], v[200:201], 0, s[30:31]
	s_mov_b32 m0, s82
	ds_read_b128 v[184:187], v152 offset:32768
	ds_read_b128 v[188:191], v152 offset:33792
	ds_read_b128 v[192:195], v151 offset:32768
	ds_read_b128 v[196:199], v151 offset:33792
	ds_read_b128 v[216:219], v150 offset:32768
	ds_read_b128 v[220:223], v150 offset:33792
	ds_read_b128 v[224:227], v149 offset:32768
	ds_read_b128 v[228:231], v149 offset:33792
	global_load_lds_dwordx4 v[232:233], off
	v_lshl_add_u64 v[232:233], v[206:207], 0, s[30:31]
	s_mov_b32 m0, s83
	s_nop 0
	global_load_lds_dwordx4 v[232:233], off
	s_waitcnt lgkmcnt(8)
	s_barrier
	s_waitcnt lgkmcnt(0)
	s_setprio 1
	s_waitcnt lgkmcnt(0)
	v_mfma_f32_16x16x32_f16 v[126:129], v[168:171], v[184:187], v[126:129]
	v_mfma_f32_16x16x32_f16 v[122:125], v[176:179], v[184:187], v[122:125]
	v_mfma_f32_16x16x32_f16 v[118:121], v[168:171], v[192:195], v[118:121]
	v_mfma_f32_16x16x32_f16 v[114:117], v[176:179], v[192:195], v[114:117]
	v_mfma_f32_16x16x32_f16 v[110:113], v[168:171], v[216:219], v[110:113]
	v_mfma_f32_16x16x32_f16 v[106:109], v[176:179], v[216:219], v[106:109]
	v_mfma_f32_16x16x32_f16 v[102:105], v[168:171], v[224:227], v[102:105]
	v_mfma_f32_16x16x32_f16 v[98:101], v[176:179], v[224:227], v[98:101]
	v_mfma_f32_16x16x32_f16 v[126:129], v[172:175], v[188:191], v[126:129]
	v_mfma_f32_16x16x32_f16 v[122:125], v[180:183], v[188:191], v[122:125]
	v_mfma_f32_16x16x32_f16 v[118:121], v[172:175], v[196:199], v[118:121]
	v_mfma_f32_16x16x32_f16 v[114:117], v[180:183], v[196:199], v[114:117]
	v_mfma_f32_16x16x32_f16 v[110:113], v[172:175], v[220:223], v[110:113]
	v_mfma_f32_16x16x32_f16 v[106:109], v[180:183], v[220:223], v[106:109]
	v_mfma_f32_16x16x32_f16 v[102:105], v[172:175], v[228:231], v[102:105]
	v_mfma_f32_16x16x32_f16 v[98:101], v[180:183], v[228:231], v[98:101]
	s_setprio 0
	s_barrier
	v_lshl_add_u64 v[252:253], v[248:249], 0, s[34:35]
	s_mov_b32 m0, s84
	ds_read_b128 v[232:235], v153
	ds_read_b128 v[236:239], v153 offset:1024
	ds_read_b128 v[240:243], v153 offset:2048
	ds_read_b128 v[244:247], v153 offset:3072
	global_load_lds_dwordx4 v[252:253], off
	v_lshl_add_u64 v[252:253], v[250:251], 0, s[34:35]
	s_mov_b32 m0, s85
	s_nop 0
	global_load_lds_dwordx4 v[252:253], off
	s_barrier
	s_waitcnt lgkmcnt(0)
	s_setprio 1
	s_waitcnt lgkmcnt(0)
	v_mfma_f32_16x16x32_f16 v[94:97], v[232:235], v[184:187], v[94:97]
	v_mfma_f32_16x16x32_f16 v[90:93], v[240:243], v[184:187], v[90:93]
	v_mfma_f32_16x16x32_f16 v[86:89], v[232:235], v[192:195], v[86:89]
	v_mfma_f32_16x16x32_f16 v[82:85], v[240:243], v[192:195], v[82:85]
	v_mfma_f32_16x16x32_f16 v[70:73], v[232:235], v[216:219], v[70:73]
	v_mfma_f32_16x16x32_f16 v[66:69], v[240:243], v[216:219], v[66:69]
	v_mfma_f32_16x16x32_f16 v[62:65], v[232:235], v[224:227], v[62:65]
	v_mfma_f32_16x16x32_f16 v[58:61], v[240:243], v[224:227], v[58:61]
	v_mfma_f32_16x16x32_f16 v[94:97], v[236:239], v[188:191], v[94:97]
	v_mfma_f32_16x16x32_f16 v[90:93], v[244:247], v[188:191], v[90:93]
	v_mfma_f32_16x16x32_f16 v[86:89], v[236:239], v[196:199], v[86:89]
	v_mfma_f32_16x16x32_f16 v[82:85], v[244:247], v[196:199], v[82:85]
	v_mfma_f32_16x16x32_f16 v[70:73], v[236:239], v[220:223], v[70:73]
	v_mfma_f32_16x16x32_f16 v[66:69], v[244:247], v[220:223], v[66:69]
	v_mfma_f32_16x16x32_f16 v[62:65], v[236:239], v[228:231], v[62:65]
	v_mfma_f32_16x16x32_f16 v[58:61], v[244:247], v[228:231], v[58:61]
	s_setprio 0
	v_lshl_add_u64 v[200:201], v[200:201], 0, s[34:35]
	s_mov_b32 m0, s86
	s_barrier
	ds_read_b128 v[184:187], v152 offset:49152
	ds_read_b128 v[188:191], v152 offset:50176
	ds_read_b128 v[192:195], v151 offset:49152
	ds_read_b128 v[196:199], v151 offset:50176
	ds_read_b128 v[216:219], v150 offset:49152
	ds_read_b128 v[220:223], v150 offset:50176
	ds_read_b128 v[224:227], v149 offset:49152
	ds_read_b128 v[228:231], v149 offset:50176
	global_load_lds_dwordx4 v[200:201], off
	v_lshl_add_u64 v[200:201], v[206:207], 0, s[34:35]
	s_mov_b32 m0, s87
	s_nop 0
	global_load_lds_dwordx4 v[200:201], off
	s_barrier
	s_waitcnt lgkmcnt(0)
	s_setprio 1
	s_waitcnt lgkmcnt(0)
	v_mfma_f32_16x16x32_f16 v[54:57], v[168:171], v[184:187], v[54:57]
	v_mfma_f32_16x16x32_f16 v[50:53], v[176:179], v[184:187], v[50:53]
	v_mfma_f32_16x16x32_f16 v[46:49], v[168:171], v[192:195], v[46:49]
	v_mfma_f32_16x16x32_f16 v[42:45], v[176:179], v[192:195], v[42:45]
	v_mfma_f32_16x16x32_f16 v[38:41], v[168:171], v[216:219], v[38:41]
	v_mfma_f32_16x16x32_f16 v[34:37], v[176:179], v[216:219], v[34:37]
	v_mfma_f32_16x16x32_f16 v[30:33], v[168:171], v[224:227], v[30:33]
	v_mfma_f32_16x16x32_f16 v[26:29], v[176:179], v[224:227], v[26:29]
	v_mfma_f32_16x16x32_f16 v[54:57], v[172:175], v[188:191], v[54:57]
	v_mfma_f32_16x16x32_f16 v[50:53], v[180:183], v[188:191], v[50:53]
	v_mfma_f32_16x16x32_f16 v[46:49], v[172:175], v[196:199], v[46:49]
	v_mfma_f32_16x16x32_f16 v[42:45], v[180:183], v[196:199], v[42:45]
	v_mfma_f32_16x16x32_f16 v[38:41], v[172:175], v[220:223], v[38:41]
	v_mfma_f32_16x16x32_f16 v[34:37], v[180:183], v[220:223], v[34:37]
	v_mfma_f32_16x16x32_f16 v[30:33], v[172:175], v[228:231], v[30:33]
	v_mfma_f32_16x16x32_f16 v[26:29], v[180:183], v[228:231], v[26:29]
	s_setprio 0
	s_barrier
	v_lshl_add_u64 v[168:169], v[248:249], 0, s[36:37]
	s_mov_b32 m0, s88
	s_nop 0
	global_load_lds_dwordx4 v[168:169], off
	v_lshl_add_u64 v[168:169], v[250:251], 0, s[36:37]
	s_mov_b32 m0, s89
	s_nop 0
	global_load_lds_dwordx4 v[168:169], off
	s_waitcnt vmcnt(6)
	s_barrier
	s_setprio 1
	v_mfma_f32_16x16x32_f16 v[22:25], v[232:235], v[184:187], v[22:25]
	v_mfma_f32_16x16x32_f16 v[18:21], v[240:243], v[184:187], v[18:21]
	v_mfma_f32_16x16x32_f16 v[14:17], v[232:235], v[192:195], v[14:17]
	v_mfma_f32_16x16x32_f16 v[10:13], v[240:243], v[192:195], v[10:13]
	v_mfma_f32_16x16x32_f16 v[6:9], v[232:235], v[216:219], v[6:9]
	v_mfma_f32_16x16x32_f16 v[2:5], v[240:243], v[216:219], v[2:5]
	v_mfma_f32_16x16x32_f16 v[74:77], v[232:235], v[224:227], v[74:77]
	v_mfma_f32_16x16x32_f16 v[78:81], v[240:243], v[224:227], v[78:81]
	v_mfma_f32_16x16x32_f16 v[22:25], v[236:239], v[188:191], v[22:25]
	v_mfma_f32_16x16x32_f16 v[18:21], v[244:247], v[188:191], v[18:21]
	v_mfma_f32_16x16x32_f16 v[14:17], v[236:239], v[196:199], v[14:17]
	v_mfma_f32_16x16x32_f16 v[10:13], v[244:247], v[196:199], v[10:13]
	v_mfma_f32_16x16x32_f16 v[6:9], v[236:239], v[220:223], v[6:9]
	v_mfma_f32_16x16x32_f16 v[2:5], v[244:247], v[220:223], v[2:5]
	v_mfma_f32_16x16x32_f16 v[74:77], v[236:239], v[228:231], v[74:77]
	v_mfma_f32_16x16x32_f16 v[78:81], v[244:247], v[228:231], v[78:81]
	s_setprio 0
	s_add_i32 s21, s21, 2
	v_lshl_add_u64 v[136:137], v[136:137], 0, s[28:29]
	v_lshl_add_u64 v[138:139], v[138:139], 0, s[28:29]
	v_lshl_add_u64 v[140:141], v[140:141], 0, s[28:29]
	s_cmp_lt_u32 s21, 28
	v_lshl_add_u64 v[142:143], v[142:143], 0, s[28:29]
	s_barrier
	s_cbranch_scc1 .LBB1_20
	s_mov_b64 s[26:27], 0xf80
	v_lshl_add_u64 v[130:131], v[132:133], 0, s[26:27]
	v_add_u32_e32 v132, 0xc000, v144
	ds_read_b128 v[136:139], v165
	ds_read_b128 v[140:143], v165 offset:1024
	ds_read_b128 v[156:159], v165 offset:2048
	ds_read_b128 v[162:165], v165 offset:3072
	v_readfirstlane_b32 s21, v132
	v_add_u32_e32 v132, 0xe000, v144
	s_mov_b32 m0, s21
	v_readfirstlane_b32 s21, v132
	global_load_lds_dwordx4 v[130:131], off
	v_lshl_add_u64 v[130:131], v[134:135], 0, s[26:27]
	s_mov_b32 m0, s21
	s_nop 0
	global_load_lds_dwordx4 v[130:131], off
	ds_read_b128 v[130:133], v152
	ds_read_b128 v[144:147], v152 offset:1024
	ds_read_b128 v[166:169], v151
	ds_read_b128 v[170:173], v151 offset:1024
	ds_read_b128 v[174:177], v150
	ds_read_b128 v[178:181], v150 offset:1024
	ds_read_b128 v[182:185], v149
	ds_read_b128 v[186:189], v149 offset:1024
	s_barrier
	s_waitcnt lgkmcnt(0)
	s_setprio 1
	s_waitcnt lgkmcnt(0)
	v_mfma_f32_16x16x32_f16 v[126:129], v[136:139], v[130:133], v[126:129]
	v_mfma_f32_16x16x32_f16 v[118:121], v[136:139], v[166:169], v[118:121]
	v_mfma_f32_16x16x32_f16 v[110:113], v[136:139], v[174:177], v[110:113]
	v_mfma_f32_16x16x32_f16 v[106:109], v[156:159], v[174:177], v[106:109]
	v_mfma_f32_16x16x32_f16 v[126:129], v[140:143], v[144:147], v[126:129]
	v_mfma_f32_16x16x32_f16 v[122:125], v[156:159], v[130:133], v[122:125]
	v_mfma_f32_16x16x32_f16 v[118:121], v[140:143], v[170:173], v[118:121]
	v_mfma_f32_16x16x32_f16 v[114:117], v[156:159], v[166:169], v[114:117]
	v_mfma_f32_16x16x32_f16 v[110:113], v[140:143], v[178:181], v[110:113]
	v_mfma_f32_16x16x32_f16 v[106:109], v[162:165], v[178:181], v[106:109]
	v_mfma_f32_16x16x32_f16 v[102:105], v[136:139], v[182:185], v[102:105]
	v_mfma_f32_16x16x32_f16 v[98:101], v[156:159], v[182:185], v[98:101]
	v_mfma_f32_16x16x32_f16 v[190:193], v[162:165], v[144:147], v[122:125]
	v_mfma_f32_16x16x32_f16 v[194:197], v[162:165], v[170:173], v[114:117]
	v_mfma_f32_16x16x32_f16 v[198:201], v[140:143], v[186:189], v[102:105]
	v_mfma_f32_16x16x32_f16 v[216:219], v[162:165], v[186:189], v[98:101]
	s_setprio 0
	s_barrier
	s_nop 1
	ds_read_b128 v[98:101], v161
	ds_read_b128 v[102:105], v161 offset:1024
	ds_read_b128 v[114:117], v161 offset:2048
	ds_read_b128 v[122:125], v161 offset:3072
	s_barrier
	s_waitcnt lgkmcnt(0)
	s_setprio 1
	s_waitcnt lgkmcnt(0)
	v_mfma_f32_16x16x32_f16 v[94:97], v[98:101], v[130:133], v[94:97]
	v_mfma_f32_16x16x32_f16 v[90:93], v[114:117], v[130:133], v[90:93]
	v_mfma_f32_16x16x32_f16 v[66:69], v[114:117], v[174:177], v[66:69]
	v_mfma_f32_16x16x32_f16 v[62:65], v[98:101], v[182:185], v[62:65]
	v_mfma_f32_16x16x32_f16 v[94:97], v[102:105], v[144:147], v[94:97]
	v_mfma_f32_16x16x32_f16 v[90:93], v[122:125], v[144:147], v[90:93]
	v_mfma_f32_16x16x32_f16 v[86:89], v[98:101], v[166:169], v[86:89]
	v_mfma_f32_16x16x32_f16 v[82:85], v[114:117], v[166:169], v[82:85]
	v_mfma_f32_16x16x32_f16 v[70:73], v[98:101], v[174:177], v[70:73]
	v_mfma_f32_16x16x32_f16 v[66:69], v[122:125], v[178:181], v[66:69]
	v_mfma_f32_16x16x32_f16 v[62:65], v[102:105], v[186:189], v[62:65]
	v_mfma_f32_16x16x32_f16 v[58:61], v[114:117], v[182:185], v[58:61]
	v_mfma_f32_16x16x32_f16 v[130:133], v[102:105], v[170:173], v[86:89]
	v_mfma_f32_16x16x32_f16 v[144:147], v[122:125], v[170:173], v[82:85]
	v_mfma_f32_16x16x32_f16 v[166:169], v[102:105], v[178:181], v[70:73]
	v_mfma_f32_16x16x32_f16 v[170:173], v[122:125], v[186:189], v[58:61]
	s_setprio 0
	s_barrier
	s_nop 1
	ds_read_b128 v[58:61], v152 offset:16384
	ds_read_b128 v[70:73], v152 offset:17408
	ds_read_b128 v[82:85], v151 offset:16384
	ds_read_b128 v[86:89], v151 offset:17408
	ds_read_b128 v[174:177], v150 offset:16384
	ds_read_b128 v[178:181], v150 offset:17408
	ds_read_b128 v[182:185], v149 offset:16384
	ds_read_b128 v[186:189], v149 offset:17408
	s_waitcnt vmcnt(4)
	s_barrier
	s_waitcnt lgkmcnt(0)
	s_setprio 1
	s_waitcnt lgkmcnt(0)
	v_mfma_f32_16x16x32_f16 v[54:57], v[136:139], v[58:61], v[54:57]
	v_mfma_f32_16x16x32_f16 v[50:53], v[156:159], v[58:61], v[50:53]
	v_mfma_f32_16x16x32_f16 v[46:49], v[136:139], v[82:85], v[46:49]
	v_mfma_f32_16x16x32_f16 v[42:45], v[156:159], v[82:85], v[42:45]
	v_mfma_f32_16x16x32_f16 v[38:41], v[136:139], v[174:177], v[38:41]
	v_mfma_f32_16x16x32_f16 v[26:29], v[156:159], v[182:185], v[26:29]
	v_mfma_f32_16x16x32_f16 v[54:57], v[140:143], v[70:73], v[54:57]
	v_mfma_f32_16x16x32_f16 v[50:53], v[162:165], v[70:73], v[50:53]
	v_mfma_f32_16x16x32_f16 v[46:49], v[140:143], v[86:89], v[46:49]
	v_mfma_f32_16x16x32_f16 v[42:45], v[162:165], v[86:89], v[42:45]
	v_mfma_f32_16x16x32_f16 v[38:41], v[140:143], v[178:181], v[38:41]
	v_mfma_f32_16x16x32_f16 v[34:37], v[156:159], v[174:177], v[34:37]
	v_mfma_f32_16x16x32_f16 v[30:33], v[136:139], v[182:185], v[30:33]
	v_mfma_f32_16x16x32_f16 v[26:29], v[162:165], v[186:189], v[26:29]
	v_mfma_f32_16x16x32_f16 v[220:223], v[162:165], v[178:181], v[34:37]
	v_mfma_f32_16x16x32_f16 v[134:137], v[140:143], v[186:189], v[30:33]
	s_setprio 0
	s_setprio 1
	v_mfma_f32_16x16x32_f16 v[2:5], v[114:117], v[174:177], v[2:5]
	v_mfma_f32_16x16x32_f16 v[22:25], v[98:101], v[58:61], v[22:25]
	v_mfma_f32_16x16x32_f16 v[10:13], v[114:117], v[82:85], v[10:13]
	v_mfma_f32_16x16x32_f16 v[6:9], v[98:101], v[174:177], v[6:9]
	v_mfma_f32_16x16x32_f16 v[160:163], v[122:125], v[178:181], v[2:5]
	v_mfma_f32_16x16x32_f16 v[2:5], v[98:101], v[182:185], v[74:77]
	v_mfma_f32_16x16x32_f16 v[22:25], v[102:105], v[70:73], v[22:25]
	v_mfma_f32_16x16x32_f16 v[18:21], v[114:117], v[58:61], v[18:21]
	v_mfma_f32_16x16x32_f16 v[14:17], v[98:101], v[82:85], v[14:17]
	v_mfma_f32_16x16x32_f16 v[10:13], v[122:125], v[86:89], v[10:13]
	v_mfma_f32_16x16x32_f16 v[6:9], v[102:105], v[178:181], v[6:9]
	v_mfma_f32_16x16x32_f16 v[174:177], v[102:105], v[186:189], v[2:5]
	v_mfma_f32_16x16x32_f16 v[2:5], v[114:117], v[182:185], v[78:81]
	v_mfma_f32_16x16x32_f16 v[138:141], v[122:125], v[70:73], v[18:21]
	v_mfma_f32_16x16x32_f16 v[156:159], v[102:105], v[86:89], v[14:17]
	v_mfma_f32_16x16x32_f16 v[178:181], v[122:125], v[186:189], v[2:5]
	s_setprio 0
	s_barrier
	s_nop 2
	ds_read_b128 v[2:5], v155
	ds_read_b128 v[14:17], v155 offset:1024
	ds_read_b128 v[182:185], v155 offset:2048
	ds_read_b128 v[186:189], v155 offset:3072
	ds_read_b128 v[18:21], v152 offset:32768
	ds_read_b128 v[30:33], v152 offset:33792
	ds_read_b128 v[34:37], v151 offset:32768
	ds_read_b128 v[74:77], v151 offset:33792
	ds_read_b128 v[78:81], v150 offset:32768
	ds_read_b128 v[224:227], v150 offset:33792
	ds_read_b128 v[228:231], v149 offset:32768
	ds_read_b128 v[232:235], v149 offset:33792
	s_waitcnt vmcnt(2)
	s_barrier
	s_waitcnt lgkmcnt(0)
	s_setprio 1
	s_waitcnt lgkmcnt(0)
	v_mfma_f32_16x16x32_f16 v[58:61], v[2:5], v[18:21], v[126:129]
	v_mfma_f32_16x16x32_f16 v[122:125], v[14:17], v[30:33], v[58:61]
	v_mfma_f32_16x16x32_f16 v[58:61], v[182:185], v[18:21], v[190:193]
	v_mfma_f32_16x16x32_f16 v[114:117], v[186:189], v[30:33], v[58:61]
	v_mfma_f32_16x16x32_f16 v[58:61], v[2:5], v[34:37], v[118:121]
	v_mfma_f32_16x16x32_f16 v[102:105], v[14:17], v[74:77], v[58:61]
	v_mfma_f32_16x16x32_f16 v[58:61], v[182:185], v[34:37], v[194:197]
	v_mfma_f32_16x16x32_f16 v[98:101], v[186:189], v[74:77], v[58:61]
	v_mfma_f32_16x16x32_f16 v[58:61], v[2:5], v[78:81], v[110:113]
	v_mfma_f32_16x16x32_f16 v[86:89], v[14:17], v[224:227], v[58:61]
	v_mfma_f32_16x16x32_f16 v[58:61], v[182:185], v[78:81], v[106:109]
	v_mfma_f32_16x16x32_f16 v[82:85], v[186:189], v[224:227], v[58:61]
	v_mfma_f32_16x16x32_f16 v[58:61], v[2:5], v[228:231], v[198:201]
	v_mfma_f32_16x16x32_f16 v[70:73], v[14:17], v[232:235], v[58:61]
	v_mfma_f32_16x16x32_f16 v[58:61], v[182:185], v[228:231], v[216:219]
	v_mfma_f32_16x16x32_f16 v[58:61], v[186:189], v[232:235], v[58:61]
	s_setprio 0
	s_barrier
	ds_read_b128 v[190:193], v153
	ds_read_b128 v[194:197], v153 offset:1024
	ds_read_b128 v[198:201], v153 offset:2048
	ds_read_b128 v[216:219], v153 offset:3072
	s_waitcnt vmcnt(0)
	s_barrier
	s_waitcnt lgkmcnt(0)
	s_setprio 1
	s_waitcnt lgkmcnt(0)
	v_mfma_f32_16x16x32_f16 v[94:97], v[190:193], v[18:21], v[94:97]
	v_mfma_f32_16x16x32_f16 v[18:21], v[198:201], v[18:21], v[90:93]
	v_mfma_f32_16x16x32_f16 v[118:121], v[216:219], v[30:33], v[18:21]
	v_mfma_f32_16x16x32_f16 v[18:21], v[190:193], v[34:37], v[130:133]
	v_mfma_f32_16x16x32_f16 v[110:113], v[194:197], v[74:77], v[18:21]
	v_mfma_f32_16x16x32_f16 v[18:21], v[198:201], v[34:37], v[144:147]
	v_mfma_f32_16x16x32_f16 v[106:109], v[216:219], v[74:77], v[18:21]
	v_mfma_f32_16x16x32_f16 v[18:21], v[190:193], v[78:81], v[166:169]
	v_mfma_f32_16x16x32_f16 v[126:129], v[194:197], v[30:33], v[94:97]
	v_mfma_f32_16x16x32_f16 v[94:97], v[194:197], v[224:227], v[18:21]
	v_mfma_f32_16x16x32_f16 v[18:21], v[198:201], v[78:81], v[66:69]
	v_mfma_f32_16x16x32_f16 v[90:93], v[216:219], v[224:227], v[18:21]
	v_mfma_f32_16x16x32_f16 v[18:21], v[190:193], v[228:231], v[62:65]
	v_mfma_f32_16x16x32_f16 v[78:81], v[194:197], v[232:235], v[18:21]
	v_mfma_f32_16x16x32_f16 v[18:21], v[198:201], v[228:231], v[170:173]
	v_mfma_f32_16x16x32_f16 v[74:77], v[216:219], v[232:235], v[18:21]
	s_setprio 0
	s_barrier
	ds_read_b128 v[130:133], v152 offset:49152
	ds_read_b128 v[142:145], v152 offset:50176
	ds_read_b128 v[152:155], v151 offset:49152
	ds_read_b128 v[164:167], v151 offset:50176
	ds_read_b128 v[168:171], v150 offset:49152
	ds_read_b128 v[224:227], v150 offset:50176
	ds_read_b128 v[228:231], v149 offset:49152
	ds_read_b128 v[146:149], v149 offset:50176
	s_barrier
	s_waitcnt lgkmcnt(0)
	s_setprio 1
	s_waitcnt lgkmcnt(0)
	v_mfma_f32_16x16x32_f16 v[18:21], v[2:5], v[130:133], v[54:57]
	v_mfma_f32_16x16x32_f16 v[66:69], v[14:17], v[142:145], v[18:21]
	v_mfma_f32_16x16x32_f16 v[18:21], v[182:185], v[130:133], v[50:53]
	v_mfma_f32_16x16x32_f16 v[50:53], v[186:189], v[142:145], v[18:21]
	v_mfma_f32_16x16x32_f16 v[18:21], v[2:5], v[152:155], v[46:49]
	v_mfma_f32_16x16x32_f16 v[46:49], v[14:17], v[164:167], v[18:21]
	v_mfma_f32_16x16x32_f16 v[18:21], v[182:185], v[152:155], v[42:45]
	v_mfma_f32_16x16x32_f16 v[34:37], v[186:189], v[164:167], v[18:21]
	v_mfma_f32_16x16x32_f16 v[18:21], v[2:5], v[168:171], v[38:41]
	v_mfma_f32_16x16x32_f16 v[2:5], v[2:5], v[228:231], v[134:137]
	v_mfma_f32_16x16x32_f16 v[30:33], v[14:17], v[224:227], v[18:21]
	v_mfma_f32_16x16x32_f16 v[18:21], v[182:185], v[168:171], v[220:223]
	v_mfma_f32_16x16x32_f16 v[14:17], v[14:17], v[146:149], v[2:5]
	v_mfma_f32_16x16x32_f16 v[2:5], v[182:185], v[228:231], v[26:29]
	v_mfma_f32_16x16x32_f16 v[18:21], v[186:189], v[224:227], v[18:21]
	v_mfma_f32_16x16x32_f16 v[2:5], v[186:189], v[146:149], v[2:5]
	s_setprio 0
	s_setprio 1
	v_mfma_f32_16x16x32_f16 v[22:25], v[190:193], v[130:133], v[22:25]
	v_mfma_f32_16x16x32_f16 v[62:65], v[194:197], v[142:145], v[22:25]
	v_mfma_f32_16x16x32_f16 v[22:25], v[198:201], v[130:133], v[138:141]
	v_mfma_f32_16x16x32_f16 v[6:9], v[190:193], v[168:171], v[6:9]
	v_mfma_f32_16x16x32_f16 v[54:57], v[216:219], v[142:145], v[22:25]
	v_mfma_f32_16x16x32_f16 v[22:25], v[190:193], v[152:155], v[156:159]
	v_mfma_f32_16x16x32_f16 v[26:29], v[194:197], v[224:227], v[6:9]
	v_mfma_f32_16x16x32_f16 v[6:9], v[198:201], v[168:171], v[160:163]
	v_mfma_f32_16x16x32_f16 v[42:45], v[194:197], v[164:167], v[22:25]
	v_mfma_f32_16x16x32_f16 v[10:13], v[198:201], v[152:155], v[10:13]
	v_mfma_f32_16x16x32_f16 v[22:25], v[216:219], v[224:227], v[6:9]
	v_mfma_f32_16x16x32_f16 v[6:9], v[190:193], v[228:231], v[174:177]
	v_mfma_f32_16x16x32_f16 v[38:41], v[216:219], v[164:167], v[10:13]
	v_mfma_f32_16x16x32_f16 v[10:13], v[194:197], v[146:149], v[6:9]
	v_mfma_f32_16x16x32_f16 v[6:9], v[198:201], v[228:231], v[178:181]
	v_mfma_f32_16x16x32_f16 v[6:9], v[216:219], v[146:149], v[6:9]
	s_setprio 0
	s_barrier
	s_and_saveexec_b64 s[26:27], s[0:1]
	s_cbranch_execz .LBB1_23
	s_barrier

.LBB1_66:
	s_or_b64 exec, exec, s[28:29]
	s_add_i32 s25, 0, 0x18000
	v_add_u32_e32 v220, s25, v222
	s_mov_b64 s[28:29], 0x80
	v_readfirstlane_b32 s30, v220
	v_add_u32_e32 v151, 0x2000, v220
	v_lshl_add_u64 v[2:3], v[2:3], 0, s[28:29]
	s_mov_b32 m0, s30
	v_readfirstlane_b32 s30, v151
	v_add_u32_e32 v152, 0x8000, v218
	s_waitcnt vmcnt(4)
	s_barrier
	global_load_lds_dwordx4 v[2:3], off
	v_lshl_add_u64 v[2:3], v[4:5], 0, s[28:29]
	s_mov_b32 m0, s30
	v_readfirstlane_b32 s30, v152
	v_add_u32_e32 v153, 0xa000, v218
	global_load_lds_dwordx4 v[2:3], off
	v_lshl_add_u64 v[2:3], v[6:7], 0, s[28:29]
	s_mov_b32 m0, s30
	v_readfirstlane_b32 s30, v153
	global_load_lds_dwordx4 v[2:3], off
	s_mov_b32 m0, s30
	s_add_i32 s30, 0, 0x1c000
	v_add_u32_e32 v221, s30, v222
	v_lshl_add_u64 v[2:3], v[8:9], 0, s[28:29]
	v_readfirstlane_b32 s31, v221
	global_load_lds_dwordx4 v[2:3], off
	v_lshl_add_u64 v[2:3], v[10:11], 0, s[28:29]
	s_mov_b32 m0, s31
	v_add_u32_e32 v154, 0x2000, v221
	global_load_lds_dwordx4 v[2:3], off
	v_lshl_add_u64 v[2:3], v[12:13], 0, s[28:29]
	v_readfirstlane_b32 s28, v154
	s_mov_b32 m0, s28
	v_lshlrev_b32_e32 v4, 6, v0
	global_load_lds_dwordx4 v[2:3], off
	v_lshlrev_b32_e32 v5, 2, v0
	v_and_b32_e32 v3, 48, v0
	v_and_b32_e32 v4, 0x3c0, v4
	v_and_b32_e32 v5, 32, v5
	v_bitop3_b32 v225, v4, v5, v3 bitop3:0x36
	v_add_u32_e32 v3, s3, v225
	v_lshrrev_b32_e32 v217, 7, v0
	v_lshlrev_b32_e32 v10, 12, v14
	s_add_u32 s0, s14, s0
	v_lshlrev_b32_e32 v11, 5, v17
	s_mov_b32 s3, 0x70000
	v_lshl_or_b32 v208, v217, 16, v10
	v_mov_b32_e32 v209, v205
	s_addc_u32 s1, s15, s1
	v_and_or_b32 v210, v11, s3, v10
	v_mov_b32_e32 v211, v205
	v_bfe_u32 v226, v0, 6, 2
	s_waitcnt vmcnt(6)
	v_lshlrev_b32_e32 v6, 13, v18
	v_lshl_add_u64 v[134:135], s[0:1], 0, v[208:209]
	v_lshl_add_u64 v[136:137], s[0:1], 0, v[210:211]
	s_add_u32 s0, s12, s26
	v_lshlrev_b32_e32 v2, 12, v226
	v_add_u32_e32 v223, s23, v225
	v_add_u32_e32 v4, s25, v225
	v_add_u32_e32 v5, s30, v225
	v_add_u32_e32 v224, 0, v225
	v_or_b32_e32 v7, 0x800, v6
	v_or_b32_e32 v8, 0x1000, v6
	v_or_b32_e32 v9, 0x1800, v6
	s_addc_u32 s1, s13, s27
	v_and_b32_e32 v1, 15, v0
	v_lshlrev_b32_e32 v214, 6, v18
	v_add_u32_e32 v202, v15, v16
	v_mov_b32_e32 v203, v205
	v_lshl_add_u64 v[138:139], s[0:1], 0, v[208:209]
	v_lshl_add_u64 v[140:141], s[0:1], 0, v[210:211]
	s_mov_b32 s3, -2
	s_mov_b64 s[0:1], 0x80080
	s_mov_b64 s[26:27], 0x100
	s_mov_b64 s[28:29], 0x80100
	s_mov_b64 s[30:31], 0x180
	s_mov_b64 s[34:35], 0x80180
	v_add_u32_e32 v156, v3, v2
	v_add_u32_e32 v145, v224, v6
	v_add_u32_e32 v144, v224, v7
	v_add_u32_e32 v143, v224, v8
	v_add_u32_e32 v142, v224, v9
	v_add_u32_e32 v155, v223, v2
	v_add_u32_e32 v148, v4, v2
	v_add_u32_e32 v146, v5, v2
	v_mov_b32_e32 v2, v205
	v_mov_b32_e32 v3, v205
	v_mov_b32_e32 v4, v205
	v_mov_b32_e32 v5, v205
	v_mov_b32_e32 v6, v205
	v_mov_b32_e32 v7, v205
	v_mov_b32_e32 v8, v205
	v_mov_b32_e32 v9, v205
	v_mov_b32_e32 v10, v205
	v_mov_b32_e32 v11, v205
	v_mov_b32_e32 v12, v205
	v_mov_b32_e32 v13, v205
	v_mov_b32_e32 v14, v205
	v_mov_b32_e32 v15, v205
	v_mov_b32_e32 v16, v205
	v_mov_b32_e32 v17, v205
	v_mov_b32_e32 v18, v205
	v_mov_b32_e32 v19, v205
	v_mov_b32_e32 v20, v205
	v_mov_b32_e32 v21, v205
	v_mov_b32_e32 v22, v205
	v_mov_b32_e32 v23, v205
	v_mov_b32_e32 v24, v205
	v_mov_b32_e32 v25, v205
	v_mov_b32_e32 v26, v205
	v_mov_b32_e32 v27, v205
	v_mov_b32_e32 v28, v205
	v_mov_b32_e32 v29, v205
	v_mov_b32_e32 v30, v205
	v_mov_b32_e32 v31, v205
	v_mov_b32_e32 v32, v205
	v_mov_b32_e32 v33, v205
	v_mov_b32_e32 v34, v205
	v_mov_b32_e32 v35, v205
	v_mov_b32_e32 v36, v205
	v_mov_b32_e32 v37, v205
	v_mov_b32_e32 v38, v205
	v_mov_b32_e32 v39, v205
	v_mov_b32_e32 v40, v205
	v_mov_b32_e32 v41, v205
	v_mov_b32_e32 v42, v205
	v_mov_b32_e32 v43, v205
	v_mov_b32_e32 v44, v205
	v_mov_b32_e32 v45, v205
	v_mov_b32_e32 v46, v205
	v_mov_b32_e32 v47, v205
	v_mov_b32_e32 v48, v205
	v_mov_b32_e32 v49, v205
	v_mov_b32_e32 v50, v205
	v_mov_b32_e32 v51, v205
	v_mov_b32_e32 v52, v205
	v_mov_b32_e32 v53, v205
	v_mov_b32_e32 v54, v205
	v_mov_b32_e32 v55, v205
	v_mov_b32_e32 v56, v205
	v_mov_b32_e32 v57, v205
	v_mov_b32_e32 v58, v205
	v_mov_b32_e32 v59, v205
	v_mov_b32_e32 v60, v205
	v_mov_b32_e32 v61, v205
	v_mov_b32_e32 v62, v205
	v_mov_b32_e32 v63, v205
	v_mov_b32_e32 v64, v205
	v_mov_b32_e32 v65, v205
	v_mov_b32_e32 v66, v205
	v_mov_b32_e32 v67, v205
	v_mov_b32_e32 v68, v205
	v_mov_b32_e32 v69, v205
	v_mov_b32_e32 v74, v205
	v_mov_b32_e32 v75, v205
	v_mov_b32_e32 v76, v205
	v_mov_b32_e32 v77, v205
	v_mov_b32_e32 v82, v205
	v_mov_b32_e32 v83, v205
	v_mov_b32_e32 v84, v205
	v_mov_b32_e32 v85, v205
	v_mov_b32_e32 v86, v205
	v_mov_b32_e32 v87, v205
	v_mov_b32_e32 v88, v205
	v_mov_b32_e32 v89, v205
	v_mov_b32_e32 v90, v205
	v_mov_b32_e32 v91, v205
	v_mov_b32_e32 v92, v205
	v_mov_b32_e32 v93, v205
	v_mov_b32_e32 v94, v205
	v_mov_b32_e32 v95, v205
	v_mov_b32_e32 v96, v205
	v_mov_b32_e32 v97, v205
	v_mov_b32_e32 v98, v205
	v_mov_b32_e32 v99, v205
	v_mov_b32_e32 v100, v205
	v_mov_b32_e32 v101, v205
	v_mov_b32_e32 v102, v205
	v_mov_b32_e32 v103, v205
	v_mov_b32_e32 v104, v205
	v_mov_b32_e32 v105, v205
	v_mov_b32_e32 v106, v205
	v_mov_b32_e32 v107, v205
	v_mov_b32_e32 v108, v205
	v_mov_b32_e32 v109, v205
	v_mov_b32_e32 v110, v205
	v_mov_b32_e32 v111, v205
	v_mov_b32_e32 v112, v205
	v_mov_b32_e32 v113, v205
	v_mov_b32_e32 v114, v205
	v_mov_b32_e32 v115, v205
	v_mov_b32_e32 v116, v205
	v_mov_b32_e32 v117, v205
	v_mov_b32_e32 v118, v205
	v_mov_b32_e32 v119, v205
	v_mov_b32_e32 v120, v205
	v_mov_b32_e32 v121, v205
	v_mov_b32_e32 v122, v205
	v_mov_b32_e32 v123, v205
	v_mov_b32_e32 v124, v205
	v_mov_b32_e32 v125, v205
	v_mov_b32_e32 v126, v205
	v_mov_b32_e32 v127, v205
	v_mov_b32_e32 v128, v205
	v_mov_b32_e32 v129, v205
	v_mov_b32_e32 v70, v205
	v_mov_b32_e32 v71, v205
	v_mov_b32_e32 v72, v205
	v_mov_b32_e32 v73, v205
	v_mov_b32_e32 v78, v205
	v_mov_b32_e32 v79, v205
	v_mov_b32_e32 v80, v205
	v_mov_b32_e32 v81, v205
	s_barrier
	s_nop 1
	v_readfirstlane_b32 s74, v216
	v_readfirstlane_b32 s75, v218
	v_readfirstlane_b32 s76, v147
	v_readfirstlane_b32 s77, v219
	v_readfirstlane_b32 s78, v149
	v_readfirstlane_b32 s79, v150
	v_readfirstlane_b32 s80, v220
	v_readfirstlane_b32 s81, v151
	v_readfirstlane_b32 s82, v152
	v_readfirstlane_b32 s83, v153
	v_readfirstlane_b32 s84, v221
	v_readfirstlane_b32 s85, v154
.LBB1_67:
	ds_read_b128 v[158:161], v156
	ds_read_b128 v[162:165], v156 offset:1024
	ds_read_b128 v[166:169], v156 offset:2048
	ds_read_b128 v[170:173], v156 offset:3072
	v_add_u32_e32 v157, 0xc000, v218
	v_lshl_add_u64 v[212:213], v[138:139], 0, v[202:203]
	v_readfirstlane_b32 s23, v157
	v_add_u32_e32 v157, 0xe000, v218
	v_lshl_add_u64 v[174:175], v[212:213], 0, s[0:1]
	s_mov_b32 m0, s23
	v_lshl_add_u64 v[250:251], v[140:141], 0, v[202:203]
	v_readfirstlane_b32 s23, v157
	global_load_lds_dwordx4 v[174:175], off
	v_lshl_add_u64 v[174:175], v[250:251], 0, s[0:1]
	s_mov_b32 m0, s23
	s_nop 0
	global_load_lds_dwordx4 v[174:175], off
	ds_read_b128 v[174:177], v145
	ds_read_b128 v[178:181], v145 offset:1024
	ds_read_b128 v[182:185], v144
	ds_read_b128 v[186:189], v144 offset:1024
	ds_read_b128 v[190:193], v143
	ds_read_b128 v[194:197], v143 offset:1024
	ds_read_b128 v[198:201], v142
	ds_read_b128 v[230:233], v142 offset:1024
	s_waitcnt lgkmcnt(8)
	s_barrier
	s_waitcnt lgkmcnt(0)
	s_setprio 1
	s_waitcnt lgkmcnt(0)
	v_mfma_f32_16x16x32_f16 v[126:129], v[158:161], v[174:177], v[126:129]
	v_mfma_f32_16x16x32_f16 v[122:125], v[166:169], v[174:177], v[122:125]
	v_mfma_f32_16x16x32_f16 v[118:121], v[158:161], v[182:185], v[118:121]
	v_mfma_f32_16x16x32_f16 v[114:117], v[166:169], v[182:185], v[114:117]
	v_mfma_f32_16x16x32_f16 v[110:113], v[158:161], v[190:193], v[110:113]
	v_mfma_f32_16x16x32_f16 v[106:109], v[166:169], v[190:193], v[106:109]
	v_mfma_f32_16x16x32_f16 v[102:105], v[158:161], v[198:201], v[102:105]
	v_mfma_f32_16x16x32_f16 v[98:101], v[166:169], v[198:201], v[98:101]
	v_mfma_f32_16x16x32_f16 v[126:129], v[162:165], v[178:181], v[126:129]
	v_mfma_f32_16x16x32_f16 v[122:125], v[170:173], v[178:181], v[122:125]
	v_mfma_f32_16x16x32_f16 v[118:121], v[162:165], v[186:189], v[118:121]
	v_mfma_f32_16x16x32_f16 v[114:117], v[170:173], v[186:189], v[114:117]
	v_mfma_f32_16x16x32_f16 v[110:113], v[162:165], v[194:197], v[110:113]
	v_mfma_f32_16x16x32_f16 v[106:109], v[170:173], v[194:197], v[106:109]
	v_mfma_f32_16x16x32_f16 v[102:105], v[162:165], v[230:233], v[102:105]
	v_mfma_f32_16x16x32_f16 v[98:101], v[170:173], v[230:233], v[98:101]
	s_setprio 0
	s_barrier
	v_lshl_add_u64 v[252:253], v[134:135], 0, v[202:203]
	v_lshl_add_u64 v[254:255], v[252:253], 0, s[26:27]
	s_mov_b32 m0, s74
	v_add_u32_e32 v157, 0x2000, v216
	ds_read_b128 v[234:237], v155
	ds_read_b128 v[238:241], v155 offset:1024
	ds_read_b128 v[242:245], v155 offset:2048
	ds_read_b128 v[246:249], v155 offset:3072
	global_load_lds_dwordx4 v[254:255], off
	v_lshl_add_u64 v[254:255], v[136:137], 0, v[202:203]
	v_readfirstlane_b32 s23, v157
	v_lshl_add_u64 v[228:229], v[254:255], 0, s[26:27]
	s_mov_b32 m0, s23
	s_nop 0
	global_load_lds_dwordx4 v[228:229], off
	s_barrier
	s_waitcnt lgkmcnt(0)
	s_setprio 1
	s_waitcnt lgkmcnt(0)
	v_mfma_f32_16x16x32_f16 v[94:97], v[234:237], v[174:177], v[94:97]
	v_mfma_f32_16x16x32_f16 v[90:93], v[242:245], v[174:177], v[90:93]
	v_mfma_f32_16x16x32_f16 v[86:89], v[234:237], v[182:185], v[86:89]
	v_mfma_f32_16x16x32_f16 v[82:85], v[242:245], v[182:185], v[82:85]
	v_mfma_f32_16x16x32_f16 v[74:77], v[234:237], v[190:193], v[74:77]
	v_mfma_f32_16x16x32_f16 v[66:69], v[242:245], v[190:193], v[66:69]
	v_mfma_f32_16x16x32_f16 v[62:65], v[234:237], v[198:201], v[62:65]
	v_mfma_f32_16x16x32_f16 v[58:61], v[242:245], v[198:201], v[58:61]
	v_mfma_f32_16x16x32_f16 v[94:97], v[238:241], v[178:181], v[94:97]
	v_mfma_f32_16x16x32_f16 v[90:93], v[246:249], v[178:181], v[90:93]
	v_mfma_f32_16x16x32_f16 v[86:89], v[238:241], v[186:189], v[86:89]
	v_mfma_f32_16x16x32_f16 v[82:85], v[246:249], v[186:189], v[82:85]
	v_mfma_f32_16x16x32_f16 v[74:77], v[238:241], v[194:197], v[74:77]
	v_mfma_f32_16x16x32_f16 v[66:69], v[246:249], v[194:197], v[66:69]
	v_mfma_f32_16x16x32_f16 v[62:65], v[238:241], v[230:233], v[62:65]
	v_mfma_f32_16x16x32_f16 v[58:61], v[246:249], v[230:233], v[58:61]
	s_setprio 0
	v_lshl_add_u64 v[228:229], v[212:213], 0, s[26:27]
	s_mov_b32 m0, s75
	s_barrier
	ds_read_b128 v[174:177], v145 offset:16384
	ds_read_b128 v[178:181], v145 offset:17408
	ds_read_b128 v[182:185], v144 offset:16384
	ds_read_b128 v[186:189], v144 offset:17408
	ds_read_b128 v[190:193], v143 offset:16384
	ds_read_b128 v[194:197], v143 offset:17408
	ds_read_b128 v[198:201], v142 offset:16384
	ds_read_b128 v[230:233], v142 offset:17408
	global_load_lds_dwordx4 v[228:229], off
	v_lshl_add_u64 v[228:229], v[250:251], 0, s[26:27]
	s_mov_b32 m0, s76
	s_nop 0
	global_load_lds_dwordx4 v[228:229], off
	s_barrier
	s_waitcnt lgkmcnt(0)
	s_setprio 1
	s_waitcnt lgkmcnt(0)
	v_mfma_f32_16x16x32_f16 v[54:57], v[158:161], v[174:177], v[54:57]
	v_mfma_f32_16x16x32_f16 v[50:53], v[166:169], v[174:177], v[50:53]
	v_mfma_f32_16x16x32_f16 v[46:49], v[158:161], v[182:185], v[46:49]
	v_mfma_f32_16x16x32_f16 v[42:45], v[166:169], v[182:185], v[42:45]
	v_mfma_f32_16x16x32_f16 v[38:41], v[158:161], v[190:193], v[38:41]
	v_mfma_f32_16x16x32_f16 v[34:37], v[166:169], v[190:193], v[34:37]
	v_mfma_f32_16x16x32_f16 v[30:33], v[158:161], v[198:201], v[30:33]
	v_mfma_f32_16x16x32_f16 v[26:29], v[166:169], v[198:201], v[26:29]
	v_mfma_f32_16x16x32_f16 v[54:57], v[162:165], v[178:181], v[54:57]
	v_mfma_f32_16x16x32_f16 v[50:53], v[170:173], v[178:181], v[50:53]
	v_mfma_f32_16x16x32_f16 v[46:49], v[162:165], v[186:189], v[46:49]
	v_mfma_f32_16x16x32_f16 v[42:45], v[170:173], v[186:189], v[42:45]
	v_mfma_f32_16x16x32_f16 v[38:41], v[162:165], v[194:197], v[38:41]
	v_mfma_f32_16x16x32_f16 v[34:37], v[170:173], v[194:197], v[34:37]
	v_mfma_f32_16x16x32_f16 v[30:33], v[162:165], v[230:233], v[30:33]
	v_mfma_f32_16x16x32_f16 v[26:29], v[170:173], v[230:233], v[26:29]
	s_setprio 0
	s_barrier
	v_add_u32_e32 v157, 0x2000, v219
	v_lshl_add_u64 v[158:159], v[252:253], 0, s[28:29]
	s_mov_b32 m0, s77
	v_readfirstlane_b32 s23, v157
	global_load_lds_dwordx4 v[158:159], off
	v_lshl_add_u64 v[158:159], v[254:255], 0, s[28:29]
	s_mov_b32 m0, s23
	s_nop 0
	global_load_lds_dwordx4 v[158:159], off
	s_waitcnt vmcnt(6)
	s_barrier
	s_setprio 1
	v_mfma_f32_16x16x32_f16 v[22:25], v[234:237], v[174:177], v[22:25]
	v_mfma_f32_16x16x32_f16 v[18:21], v[242:245], v[174:177], v[18:21]
	v_mfma_f32_16x16x32_f16 v[14:17], v[234:237], v[182:185], v[14:17]
	v_mfma_f32_16x16x32_f16 v[10:13], v[242:245], v[182:185], v[10:13]
	v_mfma_f32_16x16x32_f16 v[6:9], v[234:237], v[190:193], v[6:9]
	v_mfma_f32_16x16x32_f16 v[2:5], v[242:245], v[190:193], v[2:5]
	v_mfma_f32_16x16x32_f16 v[70:73], v[234:237], v[198:201], v[70:73]
	v_mfma_f32_16x16x32_f16 v[78:81], v[242:245], v[198:201], v[78:81]
	v_mfma_f32_16x16x32_f16 v[22:25], v[238:241], v[178:181], v[22:25]
	v_mfma_f32_16x16x32_f16 v[18:21], v[246:249], v[178:181], v[18:21]
	v_mfma_f32_16x16x32_f16 v[14:17], v[238:241], v[186:189], v[14:17]
	v_mfma_f32_16x16x32_f16 v[10:13], v[246:249], v[186:189], v[10:13]
	v_mfma_f32_16x16x32_f16 v[6:9], v[238:241], v[194:197], v[6:9]
	v_mfma_f32_16x16x32_f16 v[2:5], v[246:249], v[194:197], v[2:5]
	v_mfma_f32_16x16x32_f16 v[70:73], v[238:241], v[230:233], v[70:73]
	v_mfma_f32_16x16x32_f16 v[78:81], v[246:249], v[230:233], v[78:81]
	s_setprio 0
	s_barrier
	ds_read_b128 v[158:161], v148
	ds_read_b128 v[162:165], v148 offset:1024
	ds_read_b128 v[166:169], v148 offset:2048
	ds_read_b128 v[170:173], v148 offset:3072
	v_lshl_add_u64 v[228:229], v[212:213], 0, s[28:29]
	s_mov_b32 m0, s78
	ds_read_b128 v[174:177], v145 offset:32768
	ds_read_b128 v[178:181], v145 offset:33792
	ds_read_b128 v[182:185], v144 offset:32768
	ds_read_b128 v[186:189], v144 offset:33792
	ds_read_b128 v[190:193], v143 offset:32768
	ds_read_b128 v[194:197], v143 offset:33792
	ds_read_b128 v[198:201], v142 offset:32768
	ds_read_b128 v[230:233], v142 offset:33792
	global_load_lds_dwordx4 v[228:229], off
	v_lshl_add_u64 v[228:229], v[250:251], 0, s[28:29]
	s_mov_b32 m0, s79
	s_nop 0
	global_load_lds_dwordx4 v[228:229], off
	s_waitcnt lgkmcnt(8)
	s_barrier
	s_waitcnt lgkmcnt(0)
	s_setprio 1
	s_waitcnt lgkmcnt(0)
	v_mfma_f32_16x16x32_f16 v[126:129], v[158:161], v[174:177], v[126:129]
	v_mfma_f32_16x16x32_f16 v[122:125], v[166:169], v[174:177], v[122:125]
	v_mfma_f32_16x16x32_f16 v[118:121], v[158:161], v[182:185], v[118:121]
	v_mfma_f32_16x16x32_f16 v[114:117], v[166:169], v[182:185], v[114:117]
	v_mfma_f32_16x16x32_f16 v[110:113], v[158:161], v[190:193], v[110:113]
	v_mfma_f32_16x16x32_f16 v[106:109], v[166:169], v[190:193], v[106:109]
	v_mfma_f32_16x16x32_f16 v[102:105], v[158:161], v[198:201], v[102:105]
	v_mfma_f32_16x16x32_f16 v[98:101], v[166:169], v[198:201], v[98:101]
	v_mfma_f32_16x16x32_f16 v[126:129], v[162:165], v[178:181], v[126:129]
	v_mfma_f32_16x16x32_f16 v[122:125], v[170:173], v[178:181], v[122:125]
	v_mfma_f32_16x16x32_f16 v[118:121], v[162:165], v[186:189], v[118:121]
	v_mfma_f32_16x16x32_f16 v[114:117], v[170:173], v[186:189], v[114:117]
	v_mfma_f32_16x16x32_f16 v[110:113], v[162:165], v[194:197], v[110:113]
	v_mfma_f32_16x16x32_f16 v[106:109], v[170:173], v[194:197], v[106:109]
	v_mfma_f32_16x16x32_f16 v[102:105], v[162:165], v[230:233], v[102:105]
	v_mfma_f32_16x16x32_f16 v[98:101], v[170:173], v[230:233], v[98:101]
	s_setprio 0
	s_barrier
	v_lshl_add_u64 v[228:229], v[252:253], 0, s[30:31]
	s_mov_b32 m0, s80
	ds_read_b128 v[234:237], v146
	ds_read_b128 v[238:241], v146 offset:1024
	ds_read_b128 v[242:245], v146 offset:2048
	ds_read_b128 v[246:249], v146 offset:3072
	global_load_lds_dwordx4 v[228:229], off
	v_lshl_add_u64 v[228:229], v[254:255], 0, s[30:31]
	s_mov_b32 m0, s81
	s_nop 0
	global_load_lds_dwordx4 v[228:229], off
	s_barrier
	s_waitcnt lgkmcnt(0)
	s_setprio 1
	s_waitcnt lgkmcnt(0)
	v_mfma_f32_16x16x32_f16 v[94:97], v[234:237], v[174:177], v[94:97]
	v_mfma_f32_16x16x32_f16 v[90:93], v[242:245], v[174:177], v[90:93]
	v_mfma_f32_16x16x32_f16 v[86:89], v[234:237], v[182:185], v[86:89]
	v_mfma_f32_16x16x32_f16 v[82:85], v[242:245], v[182:185], v[82:85]
	v_mfma_f32_16x16x32_f16 v[74:77], v[234:237], v[190:193], v[74:77]
	v_mfma_f32_16x16x32_f16 v[66:69], v[242:245], v[190:193], v[66:69]
	v_mfma_f32_16x16x32_f16 v[62:65], v[234:237], v[198:201], v[62:65]
	v_mfma_f32_16x16x32_f16 v[58:61], v[242:245], v[198:201], v[58:61]
	v_mfma_f32_16x16x32_f16 v[94:97], v[238:241], v[178:181], v[94:97]
	v_mfma_f32_16x16x32_f16 v[90:93], v[246:249], v[178:181], v[90:93]
	v_mfma_f32_16x16x32_f16 v[86:89], v[238:241], v[186:189], v[86:89]
	v_mfma_f32_16x16x32_f16 v[82:85], v[246:249], v[186:189], v[82:85]
	v_mfma_f32_16x16x32_f16 v[74:77], v[238:241], v[194:197], v[74:77]
	v_mfma_f32_16x16x32_f16 v[66:69], v[246:249], v[194:197], v[66:69]
	v_mfma_f32_16x16x32_f16 v[62:65], v[238:241], v[230:233], v[62:65]
	v_mfma_f32_16x16x32_f16 v[58:61], v[246:249], v[230:233], v[58:61]
	s_setprio 0
	v_lshl_add_u64 v[212:213], v[212:213], 0, s[30:31]
	s_mov_b32 m0, s82
	s_barrier
	ds_read_b128 v[174:177], v145 offset:49152
	ds_read_b128 v[178:181], v145 offset:50176
	ds_read_b128 v[182:185], v144 offset:49152
	ds_read_b128 v[186:189], v144 offset:50176
	ds_read_b128 v[190:193], v143 offset:49152
	ds_read_b128 v[194:197], v143 offset:50176
	ds_read_b128 v[198:201], v142 offset:49152
	ds_read_b128 v[230:233], v142 offset:50176
	global_load_lds_dwordx4 v[212:213], off
	v_lshl_add_u64 v[212:213], v[250:251], 0, s[30:31]
	s_mov_b32 m0, s83
	s_nop 0
	global_load_lds_dwordx4 v[212:213], off
	s_barrier
	s_waitcnt lgkmcnt(0)
	s_setprio 1
	s_waitcnt lgkmcnt(0)
	v_mfma_f32_16x16x32_f16 v[54:57], v[158:161], v[174:177], v[54:57]
	v_mfma_f32_16x16x32_f16 v[50:53], v[166:169], v[174:177], v[50:53]
	v_mfma_f32_16x16x32_f16 v[46:49], v[158:161], v[182:185], v[46:49]
	v_mfma_f32_16x16x32_f16 v[42:45], v[166:169], v[182:185], v[42:45]
	v_mfma_f32_16x16x32_f16 v[38:41], v[158:161], v[190:193], v[38:41]
	v_mfma_f32_16x16x32_f16 v[34:37], v[166:169], v[190:193], v[34:37]
	v_mfma_f32_16x16x32_f16 v[30:33], v[158:161], v[198:201], v[30:33]
	v_mfma_f32_16x16x32_f16 v[26:29], v[166:169], v[198:201], v[26:29]
	v_mfma_f32_16x16x32_f16 v[54:57], v[162:165], v[178:181], v[54:57]
	v_mfma_f32_16x16x32_f16 v[50:53], v[170:173], v[178:181], v[50:53]
	v_mfma_f32_16x16x32_f16 v[46:49], v[162:165], v[186:189], v[46:49]
	v_mfma_f32_16x16x32_f16 v[42:45], v[170:173], v[186:189], v[42:45]
	v_mfma_f32_16x16x32_f16 v[38:41], v[162:165], v[194:197], v[38:41]
	v_mfma_f32_16x16x32_f16 v[34:37], v[170:173], v[194:197], v[34:37]
	v_mfma_f32_16x16x32_f16 v[30:33], v[162:165], v[230:233], v[30:33]
	v_mfma_f32_16x16x32_f16 v[26:29], v[170:173], v[230:233], v[26:29]
	s_setprio 0
	s_barrier
	v_lshl_add_u64 v[158:159], v[252:253], 0, s[34:35]
	s_mov_b32 m0, s84
	s_nop 0
	global_load_lds_dwordx4 v[158:159], off
	v_lshl_add_u64 v[158:159], v[254:255], 0, s[34:35]
	s_mov_b32 m0, s85
	s_nop 0
	global_load_lds_dwordx4 v[158:159], off
	s_waitcnt vmcnt(6)
	s_barrier
	s_setprio 1
	v_mfma_f32_16x16x32_f16 v[22:25], v[234:237], v[174:177], v[22:25]
	v_mfma_f32_16x16x32_f16 v[18:21], v[242:245], v[174:177], v[18:21]
	v_mfma_f32_16x16x32_f16 v[14:17], v[234:237], v[182:185], v[14:17]
	v_mfma_f32_16x16x32_f16 v[10:13], v[242:245], v[182:185], v[10:13]
	v_mfma_f32_16x16x32_f16 v[6:9], v[234:237], v[190:193], v[6:9]
	v_mfma_f32_16x16x32_f16 v[2:5], v[242:245], v[190:193], v[2:5]
	v_mfma_f32_16x16x32_f16 v[70:73], v[234:237], v[198:201], v[70:73]
	v_mfma_f32_16x16x32_f16 v[78:81], v[242:245], v[198:201], v[78:81]
	v_mfma_f32_16x16x32_f16 v[22:25], v[238:241], v[178:181], v[22:25]
	v_mfma_f32_16x16x32_f16 v[18:21], v[246:249], v[178:181], v[18:21]
	v_mfma_f32_16x16x32_f16 v[14:17], v[238:241], v[186:189], v[14:17]
	v_mfma_f32_16x16x32_f16 v[10:13], v[246:249], v[186:189], v[10:13]
	v_mfma_f32_16x16x32_f16 v[6:9], v[238:241], v[194:197], v[6:9]
	v_mfma_f32_16x16x32_f16 v[2:5], v[246:249], v[194:197], v[2:5]
	v_mfma_f32_16x16x32_f16 v[70:73], v[238:241], v[230:233], v[70:73]
	v_mfma_f32_16x16x32_f16 v[78:81], v[246:249], v[230:233], v[78:81]
	s_setprio 0
	s_add_i32 s3, s3, 2
	v_lshl_add_u64 v[134:135], v[134:135], 0, s[26:27]
	v_lshl_add_u64 v[136:137], v[136:137], 0, s[26:27]
	v_lshl_add_u64 v[138:139], v[138:139], 0, s[26:27]
	s_cmp_lt_u32 s3, 28
	v_lshl_add_u64 v[140:141], v[140:141], 0, s[26:27]
	s_barrier
	s_cbranch_scc1 .LBB1_67
	v_add_u32_e32 v147, 0xc000, v218
	s_mov_b64 s[0:1], 0xf80
	v_readfirstlane_b32 s3, v147
	v_lshl_add_u64 v[130:131], v[130:131], 0, s[0:1]
	s_mov_b32 m0, s3
	ds_read_b128 v[134:137], v156
	ds_read_b128 v[138:141], v156 offset:1024
	ds_read_b128 v[150:153], v156 offset:2048
	ds_read_b128 v[156:159], v156 offset:3072
	global_load_lds_dwordx4 v[130:131], off
	v_lshl_add_u64 v[130:131], v[132:133], 0, s[0:1]
	v_add_u32_e32 v132, 0xe000, v218
	s_nop 0
	v_readfirstlane_b32 s0, v132
	s_mov_b32 m0, s0
	s_nop 0
	global_load_lds_dwordx4 v[130:131], off
	ds_read_b128 v[130:133], v145
	ds_read_b128 v[160:163], v145 offset:1024
	ds_read_b128 v[164:167], v144
	ds_read_b128 v[168:171], v144 offset:1024
	ds_read_b128 v[172:175], v143
	ds_read_b128 v[176:179], v143 offset:1024
	ds_read_b128 v[180:183], v142
	ds_read_b128 v[184:187], v142 offset:1024
	s_barrier
	s_waitcnt lgkmcnt(0)
	s_setprio 1
	s_waitcnt lgkmcnt(0)
	v_mfma_f32_16x16x32_f16 v[126:129], v[134:137], v[130:133], v[126:129]
	v_mfma_f32_16x16x32_f16 v[118:121], v[134:137], v[164:167], v[118:121]
	v_mfma_f32_16x16x32_f16 v[110:113], v[134:137], v[172:175], v[110:113]
	v_mfma_f32_16x16x32_f16 v[106:109], v[150:153], v[172:175], v[106:109]
	v_mfma_f32_16x16x32_f16 v[126:129], v[138:141], v[160:163], v[126:129]
	v_mfma_f32_16x16x32_f16 v[122:125], v[150:153], v[130:133], v[122:125]
	v_mfma_f32_16x16x32_f16 v[118:121], v[138:141], v[168:171], v[118:121]
	v_mfma_f32_16x16x32_f16 v[114:117], v[150:153], v[164:167], v[114:117]
	v_mfma_f32_16x16x32_f16 v[110:113], v[138:141], v[176:179], v[110:113]
	v_mfma_f32_16x16x32_f16 v[106:109], v[156:159], v[176:179], v[106:109]
	v_mfma_f32_16x16x32_f16 v[102:105], v[134:137], v[180:183], v[102:105]
	v_mfma_f32_16x16x32_f16 v[98:101], v[150:153], v[180:183], v[98:101]
	v_mfma_f32_16x16x32_f16 v[188:191], v[156:159], v[160:163], v[122:125]
	v_mfma_f32_16x16x32_f16 v[192:195], v[156:159], v[168:171], v[114:117]
	v_mfma_f32_16x16x32_f16 v[196:199], v[138:141], v[184:187], v[102:105]
	v_mfma_f32_16x16x32_f16 v[230:233], v[156:159], v[184:187], v[98:101]
	s_setprio 0
	s_barrier
	s_nop 1
	ds_read_b128 v[98:101], v155
	ds_read_b128 v[102:105], v155 offset:1024
	ds_read_b128 v[114:117], v155 offset:2048
	ds_read_b128 v[122:125], v155 offset:3072
	s_barrier
	s_waitcnt lgkmcnt(0)
	s_setprio 1
	s_waitcnt lgkmcnt(0)
	v_mfma_f32_16x16x32_f16 v[94:97], v[98:101], v[130:133], v[94:97]
	v_mfma_f32_16x16x32_f16 v[90:93], v[114:117], v[130:133], v[90:93]
	v_mfma_f32_16x16x32_f16 v[74:77], v[98:101], v[172:175], v[74:77]
	v_mfma_f32_16x16x32_f16 v[66:69], v[114:117], v[172:175], v[66:69]
	v_mfma_f32_16x16x32_f16 v[62:65], v[98:101], v[180:183], v[62:65]
	v_mfma_f32_16x16x32_f16 v[94:97], v[102:105], v[160:163], v[94:97]
	v_mfma_f32_16x16x32_f16 v[90:93], v[122:125], v[160:163], v[90:93]
	v_mfma_f32_16x16x32_f16 v[86:89], v[98:101], v[164:167], v[86:89]
	v_mfma_f32_16x16x32_f16 v[82:85], v[114:117], v[164:167], v[82:85]
	v_mfma_f32_16x16x32_f16 v[74:77], v[102:105], v[176:179], v[74:77]
	v_mfma_f32_16x16x32_f16 v[66:69], v[122:125], v[176:179], v[66:69]
	v_mfma_f32_16x16x32_f16 v[62:65], v[102:105], v[184:187], v[62:65]
	v_mfma_f32_16x16x32_f16 v[58:61], v[114:117], v[180:183], v[58:61]
	v_mfma_f32_16x16x32_f16 v[130:133], v[102:105], v[168:171], v[86:89]
	v_mfma_f32_16x16x32_f16 v[160:163], v[122:125], v[168:171], v[82:85]
	v_mfma_f32_16x16x32_f16 v[164:167], v[122:125], v[184:187], v[58:61]
	s_setprio 0
	s_barrier
	s_nop 2
	ds_read_b128 v[58:61], v145 offset:16384
	ds_read_b128 v[82:85], v145 offset:17408
	ds_read_b128 v[86:89], v144 offset:16384
	ds_read_b128 v[168:171], v144 offset:17408
	ds_read_b128 v[172:175], v143 offset:16384
	ds_read_b128 v[176:179], v143 offset:17408
	ds_read_b128 v[180:183], v142 offset:16384
	ds_read_b128 v[184:187], v142 offset:17408
	s_waitcnt vmcnt(4)
	s_barrier
	s_waitcnt lgkmcnt(0)
	s_setprio 1
	s_waitcnt lgkmcnt(0)
	v_mfma_f32_16x16x32_f16 v[54:57], v[134:137], v[58:61], v[54:57]
	v_mfma_f32_16x16x32_f16 v[50:53], v[150:153], v[58:61], v[50:53]
	v_mfma_f32_16x16x32_f16 v[46:49], v[134:137], v[86:89], v[46:49]
	v_mfma_f32_16x16x32_f16 v[42:45], v[150:153], v[86:89], v[42:45]
	v_mfma_f32_16x16x32_f16 v[38:41], v[134:137], v[172:175], v[38:41]
	v_mfma_f32_16x16x32_f16 v[26:29], v[150:153], v[180:183], v[26:29]
	v_mfma_f32_16x16x32_f16 v[54:57], v[138:141], v[82:85], v[54:57]
	v_mfma_f32_16x16x32_f16 v[50:53], v[156:159], v[82:85], v[50:53]
	v_mfma_f32_16x16x32_f16 v[46:49], v[138:141], v[168:171], v[46:49]
	v_mfma_f32_16x16x32_f16 v[42:45], v[156:159], v[168:171], v[42:45]
	v_mfma_f32_16x16x32_f16 v[38:41], v[138:141], v[176:179], v[38:41]
	v_mfma_f32_16x16x32_f16 v[34:37], v[150:153], v[172:175], v[34:37]
	v_mfma_f32_16x16x32_f16 v[30:33], v[134:137], v[180:183], v[30:33]
	v_mfma_f32_16x16x32_f16 v[26:29], v[156:159], v[184:187], v[26:29]
	v_mfma_f32_16x16x32_f16 v[234:237], v[156:159], v[176:179], v[34:37]
	v_mfma_f32_16x16x32_f16 v[134:137], v[138:141], v[184:187], v[30:33]
	s_setprio 0
	s_setprio 1
	v_mfma_f32_16x16x32_f16 v[2:5], v[114:117], v[172:175], v[2:5]
	v_mfma_f32_16x16x32_f16 v[22:25], v[98:101], v[58:61], v[22:25]
	v_mfma_f32_16x16x32_f16 v[14:17], v[98:101], v[86:89], v[14:17]
	v_mfma_f32_16x16x32_f16 v[10:13], v[114:117], v[86:89], v[10:13]
	v_mfma_f32_16x16x32_f16 v[6:9], v[98:101], v[172:175], v[6:9]
	v_mfma_f32_16x16x32_f16 v[154:157], v[122:125], v[176:179], v[2:5]
	v_mfma_f32_16x16x32_f16 v[2:5], v[98:101], v[180:183], v[70:73]
	v_mfma_f32_16x16x32_f16 v[22:25], v[102:105], v[82:85], v[22:25]
	v_mfma_f32_16x16x32_f16 v[18:21], v[114:117], v[58:61], v[18:21]
	v_mfma_f32_16x16x32_f16 v[150:153], v[102:105], v[168:171], v[14:17]
	v_mfma_f32_16x16x32_f16 v[10:13], v[122:125], v[168:171], v[10:13]
	v_mfma_f32_16x16x32_f16 v[6:9], v[102:105], v[176:179], v[6:9]
	v_mfma_f32_16x16x32_f16 v[168:171], v[102:105], v[184:187], v[2:5]
	v_mfma_f32_16x16x32_f16 v[2:5], v[114:117], v[180:183], v[78:81]
	v_mfma_f32_16x16x32_f16 v[138:141], v[122:125], v[82:85], v[18:21]
	v_mfma_f32_16x16x32_f16 v[172:175], v[122:125], v[184:187], v[2:5]
	s_setprio 0
	s_barrier
	s_nop 3
	ds_read_b128 v[2:5], v148
	ds_read_b128 v[14:17], v148 offset:1024
	ds_read_b128 v[176:179], v148 offset:2048
	ds_read_b128 v[180:183], v148 offset:3072
	ds_read_b128 v[18:21], v145 offset:32768
	ds_read_b128 v[30:33], v145 offset:33792
	ds_read_b128 v[34:37], v144 offset:32768
	ds_read_b128 v[78:81], v144 offset:33792
	ds_read_b128 v[184:187], v143 offset:32768
	ds_read_b128 v[238:241], v143 offset:33792
	ds_read_b128 v[242:245], v142 offset:32768
	ds_read_b128 v[246:249], v142 offset:33792
	s_waitcnt vmcnt(2)
	s_barrier
	s_waitcnt lgkmcnt(0)
	s_setprio 1
	s_waitcnt lgkmcnt(0)
	v_mfma_f32_16x16x32_f16 v[58:61], v[2:5], v[18:21], v[126:129]
	v_mfma_f32_16x16x32_f16 v[122:125], v[14:17], v[30:33], v[58:61]
	v_mfma_f32_16x16x32_f16 v[58:61], v[176:179], v[18:21], v[188:191]
	v_mfma_f32_16x16x32_f16 v[114:117], v[180:183], v[30:33], v[58:61]
	v_mfma_f32_16x16x32_f16 v[58:61], v[2:5], v[34:37], v[118:121]
	v_mfma_f32_16x16x32_f16 v[102:105], v[14:17], v[78:81], v[58:61]
	v_mfma_f32_16x16x32_f16 v[58:61], v[176:179], v[34:37], v[192:195]
	v_mfma_f32_16x16x32_f16 v[98:101], v[180:183], v[78:81], v[58:61]
	v_mfma_f32_16x16x32_f16 v[58:61], v[2:5], v[184:187], v[110:113]
	v_mfma_f32_16x16x32_f16 v[86:89], v[14:17], v[238:241], v[58:61]
	v_mfma_f32_16x16x32_f16 v[58:61], v[176:179], v[184:187], v[106:109]
	v_mfma_f32_16x16x32_f16 v[82:85], v[180:183], v[238:241], v[58:61]
	v_mfma_f32_16x16x32_f16 v[58:61], v[2:5], v[242:245], v[196:199]
	v_mfma_f32_16x16x32_f16 v[70:73], v[14:17], v[246:249], v[58:61]
	v_mfma_f32_16x16x32_f16 v[58:61], v[176:179], v[242:245], v[230:233]
	v_mfma_f32_16x16x32_f16 v[58:61], v[180:183], v[246:249], v[58:61]
	s_setprio 0
	s_barrier
	ds_read_b128 v[188:191], v146
	ds_read_b128 v[192:195], v146 offset:1024
	ds_read_b128 v[196:199], v146 offset:2048
	ds_read_b128 v[146:149], v146 offset:3072
	s_waitcnt vmcnt(0)
	s_barrier
	s_waitcnt lgkmcnt(0)
	s_setprio 1
	s_waitcnt lgkmcnt(0)
	v_mfma_f32_16x16x32_f16 v[94:97], v[188:191], v[18:21], v[94:97]
	v_mfma_f32_16x16x32_f16 v[18:21], v[196:199], v[18:21], v[90:93]
	v_mfma_f32_16x16x32_f16 v[118:121], v[146:149], v[30:33], v[18:21]
	v_mfma_f32_16x16x32_f16 v[18:21], v[188:191], v[34:37], v[130:133]
	v_mfma_f32_16x16x32_f16 v[110:113], v[192:195], v[78:81], v[18:21]
	v_mfma_f32_16x16x32_f16 v[18:21], v[196:199], v[34:37], v[160:163]
	v_mfma_f32_16x16x32_f16 v[106:109], v[146:149], v[78:81], v[18:21]
	v_mfma_f32_16x16x32_f16 v[18:21], v[188:191], v[184:187], v[74:77]
	v_mfma_f32_16x16x32_f16 v[126:129], v[192:195], v[30:33], v[94:97]
	v_mfma_f32_16x16x32_f16 v[94:97], v[192:195], v[238:241], v[18:21]
	v_mfma_f32_16x16x32_f16 v[18:21], v[196:199], v[184:187], v[66:69]
	v_mfma_f32_16x16x32_f16 v[90:93], v[146:149], v[238:241], v[18:21]
	v_mfma_f32_16x16x32_f16 v[18:21], v[188:191], v[242:245], v[62:65]
	v_mfma_f32_16x16x32_f16 v[78:81], v[192:195], v[246:249], v[18:21]
	v_mfma_f32_16x16x32_f16 v[18:21], v[196:199], v[242:245], v[164:167]
	v_mfma_f32_16x16x32_f16 v[74:77], v[146:149], v[246:249], v[18:21]
	s_setprio 0
	s_barrier
	ds_read_b128 v[130:133], v145 offset:49152
	ds_read_b128 v[158:161], v145 offset:50176
	ds_read_b128 v[162:165], v144 offset:49152
	ds_read_b128 v[184:187], v144 offset:50176
	ds_read_b128 v[230:233], v143 offset:49152
	ds_read_b128 v[238:241], v143 offset:50176
	ds_read_b128 v[242:245], v142 offset:49152
	ds_read_b128 v[142:145], v142 offset:50176
	s_barrier
	s_waitcnt lgkmcnt(0)
	s_setprio 1
	s_waitcnt lgkmcnt(0)
	v_mfma_f32_16x16x32_f16 v[18:21], v[2:5], v[130:133], v[54:57]
	v_mfma_f32_16x16x32_f16 v[66:69], v[14:17], v[158:161], v[18:21]
	v_mfma_f32_16x16x32_f16 v[18:21], v[176:179], v[130:133], v[50:53]
	v_mfma_f32_16x16x32_f16 v[50:53], v[180:183], v[158:161], v[18:21]
	v_mfma_f32_16x16x32_f16 v[18:21], v[2:5], v[162:165], v[46:49]
	v_mfma_f32_16x16x32_f16 v[46:49], v[14:17], v[184:187], v[18:21]
	v_mfma_f32_16x16x32_f16 v[18:21], v[176:179], v[162:165], v[42:45]
	v_mfma_f32_16x16x32_f16 v[34:37], v[180:183], v[184:187], v[18:21]
	v_mfma_f32_16x16x32_f16 v[18:21], v[2:5], v[230:233], v[38:41]
	v_mfma_f32_16x16x32_f16 v[2:5], v[2:5], v[242:245], v[134:137]
	v_mfma_f32_16x16x32_f16 v[30:33], v[14:17], v[238:241], v[18:21]
	v_mfma_f32_16x16x32_f16 v[18:21], v[176:179], v[230:233], v[234:237]
	v_mfma_f32_16x16x32_f16 v[14:17], v[14:17], v[142:145], v[2:5]
	v_mfma_f32_16x16x32_f16 v[2:5], v[176:179], v[242:245], v[26:29]
	v_mfma_f32_16x16x32_f16 v[18:21], v[180:183], v[238:241], v[18:21]
	v_mfma_f32_16x16x32_f16 v[2:5], v[180:183], v[142:145], v[2:5]
	s_setprio 0
	s_setprio 1
	v_mfma_f32_16x16x32_f16 v[22:25], v[188:191], v[130:133], v[22:25]
	v_mfma_f32_16x16x32_f16 v[62:65], v[192:195], v[158:161], v[22:25]
	v_mfma_f32_16x16x32_f16 v[22:25], v[196:199], v[130:133], v[138:141]
	v_mfma_f32_16x16x32_f16 v[6:9], v[188:191], v[230:233], v[6:9]
	v_mfma_f32_16x16x32_f16 v[54:57], v[146:149], v[158:161], v[22:25]
	v_mfma_f32_16x16x32_f16 v[22:25], v[188:191], v[162:165], v[150:153]
	v_mfma_f32_16x16x32_f16 v[26:29], v[192:195], v[238:241], v[6:9]
	v_mfma_f32_16x16x32_f16 v[6:9], v[196:199], v[230:233], v[154:157]
	v_mfma_f32_16x16x32_f16 v[42:45], v[192:195], v[184:187], v[22:25]
	v_mfma_f32_16x16x32_f16 v[10:13], v[196:199], v[162:165], v[10:13]
	v_mfma_f32_16x16x32_f16 v[22:25], v[146:149], v[238:241], v[6:9]
	v_mfma_f32_16x16x32_f16 v[6:9], v[188:191], v[242:245], v[168:171]
	v_mfma_f32_16x16x32_f16 v[38:41], v[146:149], v[184:187], v[10:13]
	v_mfma_f32_16x16x32_f16 v[10:13], v[192:195], v[142:145], v[6:9]
	v_mfma_f32_16x16x32_f16 v[6:9], v[196:199], v[242:245], v[172:175]
	v_mfma_f32_16x16x32_f16 v[6:9], v[146:149], v[142:145], v[6:9]
	s_setprio 0
	s_movk_i32 s0, 0x100
	v_cmp_gt_u32_e64 s[0:1], s0, v0
	s_barrier
	s_and_saveexec_b64 s[26:27], s[0:1]
	s_cbranch_execz .LBB1_70
	s_barrier

	.amdhsa_kernel _Z8gemm_qkvPKDF16_S0_PKfS2_S2_PDF16_S3_S3_
		.amdhsa_group_segment_fixed_size 0
		.amdhsa_private_segment_fixed_size 0
		.amdhsa_kernarg_size 64
		.amdhsa_user_sgpr_count 2
		.amdhsa_user_sgpr_dispatch_ptr 0
		.amdhsa_user_sgpr_queue_ptr 0
		.amdhsa_user_sgpr_kernarg_segment_ptr 1
		.amdhsa_user_sgpr_dispatch_id 0
		.amdhsa_user_sgpr_kernarg_preload_length 0
		.amdhsa_user_sgpr_kernarg_preload_offset 0
		.amdhsa_user_sgpr_private_segment_size 0
		.amdhsa_uses_dynamic_stack 0
		.amdhsa_enable_private_segment 0
		.amdhsa_system_sgpr_workgroup_id_x 1
		.amdhsa_system_sgpr_workgroup_id_y 0
		.amdhsa_system_sgpr_workgroup_id_z 0
		.amdhsa_system_sgpr_workgroup_info 0
		.amdhsa_system_vgpr_workitem_id 0
		.amdhsa_next_free_vgpr 256
		.amdhsa_next_free_sgpr 90
		.amdhsa_accum_offset 256
		.amdhsa_reserve_vcc 1
		.amdhsa_float_round_mode_32 0
		.amdhsa_float_round_mode_16_64 0
		.amdhsa_float_denorm_mode_32 3
		.amdhsa_float_denorm_mode_16_64 3
		.amdhsa_dx10_clamp 1
		.amdhsa_ieee_mode 1
		.amdhsa_fp16_overflow 0
		.amdhsa_tg_split 0
		.amdhsa_exception_fp_ieee_invalid_op 0
		.amdhsa_exception_fp_denorm_src 0
		.amdhsa_exception_fp_ieee_div_zero 0
		.amdhsa_exception_fp_ieee_overflow 0
		.amdhsa_exception_fp_ieee_underflow 0
		.amdhsa_exception_fp_ieee_inexact 0
		.amdhsa_exception_int_div_zero 0
	.end_amdhsa_kernel

amdhsa.kernels:
  - .agpr_count:     0
    .args:
      - .actual_access:  read_only
        .address_space:  global
        .offset:         0
        .size:           8
        .value_kind:     global_buffer
      - .actual_access:  write_only
        .address_space:  global
        .offset:         8
        .size:           8
        .value_kind:     global_buffer
      - .offset:         16
        .size:           8
        .value_kind:     by_value
      - .actual_access:  read_only
        .address_space:  global
        .offset:         24
        .size:           8
        .value_kind:     global_buffer
      - .actual_access:  write_only
        .address_space:  global
        .offset:         32
        .size:           8
        .value_kind:     global_buffer
      - .offset:         40
        .size:           8
        .value_kind:     by_value
      - .actual_access:  read_only
        .address_space:  global
        .offset:         48
        .size:           8
        .value_kind:     global_buffer
      - .actual_access:  write_only
        .address_space:  global
        .offset:         56
        .size:           8
        .value_kind:     global_buffer
      - .offset:         64
        .size:           8
        .value_kind:     by_value
      - .offset:         72
        .size:           4
        .value_kind:     hidden_block_count_x
      - .offset:         76
        .size:           4
        .value_kind:     hidden_block_count_y
      - .offset:         80
        .size:           4
        .value_kind:     hidden_block_count_z
      - .offset:         84
        .size:           2
        .value_kind:     hidden_group_size_x
      - .offset:         86
        .size:           2
        .value_kind:     hidden_group_size_y
      - .offset:         88
        .size:           2
        .value_kind:     hidden_group_size_z
      - .offset:         90
        .size:           2
        .value_kind:     hidden_remainder_x
      - .offset:         92
        .size:           2
        .value_kind:     hidden_remainder_y
      - .offset:         94
        .size:           2
        .value_kind:     hidden_remainder_z
      - .offset:         112
        .size:           8
        .value_kind:     hidden_global_offset_x
      - .offset:         120
        .size:           8
        .value_kind:     hidden_global_offset_y
      - .offset:         128
        .size:           8
        .value_kind:     hidden_global_offset_z
      - .offset:         136
        .size:           2
        .value_kind:     hidden_grid_dims
    .group_segment_fixed_size: 0
    .kernarg_segment_align: 8
    .kernarg_segment_size: 328
    .language:       OpenCL C
    .language_version:
      - 2
      - 0
    .max_flat_workgroup_size: 256
    .name:           _Z12cvt3_f32_f16PKfPDF16_lS0_S1_lS0_S1_l
    .private_segment_fixed_size: 0
    .sgpr_count:     34
    .sgpr_spill_count: 0
    .symbol:         _Z12cvt3_f32_f16PKfPDF16_lS0_S1_lS0_S1_l.kd
    .uniform_work_group_size: 1
    .uses_dynamic_stack: false
    .vgpr_count:     16
    .vgpr_spill_count: 0
    .wavefront_size: 64
  - .agpr_count:     0
    .args:
      - .address_space:  global
        .offset:         0
        .size:           8
        .value_kind:     global_buffer
      - .address_space:  global
        .offset:         8
        .size:           8
        .value_kind:     global_buffer
      - .actual_access:  read_only
        .address_space:  global
        .offset:         16
        .size:           8
        .value_kind:     global_buffer
      - .actual_access:  read_only
        .address_space:  global
        .offset:         24
        .size:           8
        .value_kind:     global_buffer
      - .actual_access:  read_only
        .address_space:  global
        .offset:         32
        .size:           8
        .value_kind:     global_buffer
      - .actual_access:  write_only
        .address_space:  global
        .offset:         40
        .size:           8
        .value_kind:     global_buffer
      - .actual_access:  write_only
        .address_space:  global
        .offset:         48
        .size:           8
        .value_kind:     global_buffer
      - .actual_access:  write_only
        .address_space:  global
        .offset:         56
        .size:           8
        .value_kind:     global_buffer
    .group_segment_fixed_size: 0
    .kernarg_segment_align: 8
    .kernarg_segment_size: 64
    .language:       OpenCL C
    .language_version:
      - 2
      - 0
    .max_flat_workgroup_size: 512
    .name:           _Z8gemm_qkvPKDF16_S0_PKfS2_S2_PDF16_S3_S3_
    .private_segment_fixed_size: 0
    .sgpr_count:     96
    .sgpr_spill_count: 0
    .symbol:         _Z8gemm_qkvPKDF16_S0_PKfS2_S2_PDF16_S3_S3_.kd
    .uniform_work_group_size: 1
    .uses_dynamic_stack: false
    .vgpr_count:     256
    .vgpr_spill_count: 0
    .wavefront_size: 64
  - .agpr_count:     0
    .args:
      - .address_space:  global
        .offset:         0
        .size:           8
        .value_kind:     global_buffer
      - .address_space:  global
        .offset:         8
        .size:           8
        .value_kind:     global_buffer
      - .actual_access:  read_only
        .address_space:  global
        .offset:         16
        .size:           8
        .value_kind:     global_buffer
      - .actual_access:  write_only
        .address_space:  global
        .offset:         24
        .size:           8
        .value_kind:     global_buffer
    .group_segment_fixed_size: 0
    .kernarg_segment_align: 8
    .kernarg_segment_size: 32
    .language:       OpenCL C
    .language_version:
      - 2
      - 0
    .max_flat_workgroup_size: 512
    .name:           _Z9gemm_projPKDF16_S0_PKfPf
    .private_segment_fixed_size: 0
    .sgpr_count:     54
    .sgpr_spill_count: 0
    .symbol:         _Z9gemm_projPKDF16_S0_PKfPf.kd
    .uniform_work_group_size: 1
    .uses_dynamic_stack: false
    .vgpr_count:     184
    .vgpr_spill_count: 0
    .wavefront_size: 64
  - .agpr_count:     256
    .args:
      - .address_space:  global
        .offset:         0
        .size:           8
        .value_kind:     global_buffer
      - .address_space:  global
        .offset:         8
        .size:           8
        .value_kind:     global_buffer
      - .address_space:  global
        .offset:         16
        .size:           8
        .value_kind:     global_buffer
      - .actual_access:  write_only
        .address_space:  global
        .offset:         24
        .size:           8
        .value_kind:     global_buffer
      - .offset:         32
        .size:           4
        .value_kind:     hidden_block_count_x
      - .offset:         36
        .size:           4
        .value_kind:     hidden_block_count_y
      - .offset:         40
        .size:           4
        .value_kind:     hidden_block_count_z
      - .offset:         44
        .size:           2
        .value_kind:     hidden_group_size_x
      - .offset:         46
        .size:           2
        .value_kind:     hidden_group_size_y
      - .offset:         48
        .size:           2
        .value_kind:     hidden_group_size_z
      - .offset:         50
        .size:           2
        .value_kind:     hidden_remainder_x
      - .offset:         52
        .size:           2
        .value_kind:     hidden_remainder_y
      - .offset:         54
        .size:           2
        .value_kind:     hidden_remainder_z
      - .offset:         72
        .size:           8
        .value_kind:     hidden_global_offset_x
      - .offset:         80
        .size:           8
        .value_kind:     hidden_global_offset_y
      - .offset:         88
        .size:           8
        .value_kind:     hidden_global_offset_z
      - .offset:         96
        .size:           2
        .value_kind:     hidden_grid_dims
      - .offset:         152
        .size:           4
        .value_kind:     hidden_dynamic_lds_size
    .group_segment_fixed_size: 0
    .kernarg_segment_align: 8
    .kernarg_segment_size: 288
    .language:       OpenCL C
    .language_version:
      - 2
      - 0
    .max_flat_workgroup_size: 256
    .name:           attn_fwd_pwg4x64
    .private_segment_fixed_size: 0
    .sgpr_count:     106
    .sgpr_spill_count: 0
    .symbol:         attn_fwd_pwg4x64.kd
    .uniform_work_group_size: 1
    .uses_dynamic_stack: false
    .vgpr_count:     508
    .vgpr_spill_count: 0
    .wavefront_size: 64
